# speedup vs baseline: 1.0562x; 1.0395x over previous
.LBB2_329:
	s_or_b64 exec, exec, s[4:5]
	s_lshl_b32 s98, s96, 8
	v_ashrrev_i32_e32 v154, 8, v148
	v_and_b32_e32 v152, 15, v148
	v_and_b32_e32 v150, 63, v148
	v_lshlrev_b32_e32 v151, 6, v154
	v_or_b32_e32 v2, s98, v152
	v_and_b32_e32 v146, 48, v148
	v_mov_b32_e32 v147, v163
	v_cmp_gt_u32_e64 s[4:5], 32, v150
	v_add_u32_e32 v28, v2, v151
	v_lshl_add_u64 v[26:27], s[40:41], 0, v[146:147]
	v_mov_b32_e32 v2, 0
	v_mov_b32_e32 v6, 0
	v_mov_b32_e32 v7, 0
	v_mov_b32_e32 v8, 0
	v_mov_b32_e32 v9, 0
	s_barrier
	v_lshlrev_b32_e32 v248, 4, v149
	v_lshl_or_b32 v249, s55, 8, v152
	v_add_u32_e32 v249, v249, v248
	v_lshl_add_u32 v248, s0, 13, v249
	v_lshlrev_b32_e32 v248, 2, v248
	v_mov_b32_e32 v246, 0
	v_mov_b32_e32 v247, 0
	v_cmp_gt_i32_e32 vcc, s86, v249
	s_and_saveexec_b64 s[10:11], vcc
	global_load_dword v246, v248, s[38:39]
	s_or_b64 exec, exec, s[10:11]
	v_add_u32_e32 v249, 0x80, v249
	v_cmp_gt_i32_e32 vcc, s86, v249
	s_and_saveexec_b64 s[10:11], vcc
	global_load_dword v247, v248, s[38:39] offset:512
	s_or_b64 exec, exec, s[10:11]
	s_and_saveexec_b64 s[10:11], s[4:5]
	s_cbranch_execz .LBB2_331
	v_ashrrev_i32_e32 v29, 31, v28
	v_lshlrev_b64 v[4:5], 5, v[28:29]
	v_lshl_add_u64 v[4:5], v[26:27], 0, v[4:5]
	global_load_dwordx4 v[6:9], v[4:5], off

.LBB2_355:
	s_or_b64 exec, exec, s[52:53]
	s_add_u32 s52, s92, 0x80
	s_addc_u32 s53, s93, 0
	s_add_i32 s82, 0, 0x18000
	s_add_i32 s58, s82, s57
	s_waitcnt vmcnt(8)
	v_mfma_f32_16x16x32_f16 v[102:105], v[30:33], v[6:9], 0
	s_mov_b32 m0, s58
	s_waitcnt vmcnt(4)
	v_lshl_add_u32 v248, v149, 4, v152
	v_lshlrev_b32_e32 v248, 2, v248
	v_add_u32_e32 v248, 0x20000, v248
	ds_write_b32 v248, v246
	ds_write_b32 v248, v247 offset:512
	s_barrier
	v_mfma_f32_16x16x32_f16 v[98:101], v[26:29], v[6:9], 0
	v_mfma_f32_16x16x32_f16 v[126:129], v[30:33], v[2:5], 0
	v_mfma_f32_16x16x32_f16 v[122:125], v[26:29], v[2:5], 0
	v_mfma_f32_16x16x32_f16 v[118:121], v[30:33], v[14:17], 0
	v_mfma_f32_16x16x32_f16 v[110:113], v[30:33], v[10:13], 0
	v_mfma_f32_16x16x32_f16 v[94:97], v[142:145], v[6:9], 0
	v_mfma_f32_16x16x32_f16 v[90:93], v[138:141], v[6:9], 0
	v_mfma_f32_16x16x32_f16 v[86:89], v[142:145], v[2:5], 0
	v_mfma_f32_16x16x32_f16 v[82:85], v[138:141], v[2:5], 0
	v_mfma_f32_16x16x32_f16 v[62:65], v[30:33], v[22:25], 0
	v_mfma_f32_16x16x32_f16 v[54:57], v[30:33], v[18:21], 0
	v_mfma_f32_16x16x32_f16 v[46:49], v[30:33], v[134:137], 0
	v_mfma_f32_16x16x32_f16 v[38:41], v[30:33], v[130:133], 0
	v_mfma_f32_16x16x32_f16 v[30:33], v[26:29], v[130:133], 0
	v_mfma_f32_16x16x32_f16 v[6:9], v[142:145], v[130:133], 0
	v_mfma_f32_16x16x32_f16 v[2:5], v[138:141], v[130:133], 0
	v_lshl_add_u64 v[130:131], s[52:53], 0, v[162:163]
	s_add_u32 s52, s52, 0x20000
	global_load_lds_dwordx4 v[130:131], off
	s_addc_u32 s53, s53, 0
	s_add_i32 m0, s58, 0x2000
	s_add_u32 s58, s90, 0x80
	s_addc_u32 s59, s91, 0
	v_lshl_add_u64 v[130:131], s[52:53], 0, v[162:163]
	s_add_i32 s52, s97, 0x8000
	global_load_lds_dwordx4 v[130:131], off
	v_lshl_add_u64 v[130:131], s[58:59], 0, v[162:163]
	s_add_u32 s58, s58, 0x20000
	s_addc_u32 s59, s59, 0
	s_mov_b32 m0, s52
	s_add_i32 s53, s97, 0xa000
	global_load_lds_dwordx4 v[130:131], off
	v_lshl_add_u64 v[130:131], s[58:59], 0, v[162:163]
	s_add_u32 s58, s92, 0x40080
	s_addc_u32 s59, s93, 0
	s_add_i32 s83, 0, 0x1c000
	s_mov_b32 m0, s53
	s_add_i32 s57, s83, s57
	global_load_lds_dwordx4 v[130:131], off
	v_lshl_add_u64 v[130:131], s[58:59], 0, v[162:163]
	s_add_u32 s58, s58, 0x20000
	s_mov_b32 m0, s57
	s_addc_u32 s59, s59, 0
	global_load_lds_dwordx4 v[130:131], off
	s_add_i32 m0, s57, 0x2000
	v_lshl_add_u64 v[130:131], s[58:59], 0, v[162:163]
	global_load_lds_dwordx4 v[130:131], off
	v_lshlrev_b32_e32 v132, 2, v152
	v_lshlrev_b32_e32 v130, 6, v152
	v_and_b32_e32 v131, 32, v132
	v_bitop3_b32 v130, v130, v131, v146 bitop3:0x36
	s_add_i32 s57, 0, 0x10000
	v_add_u32_e32 v131, s57, v130
	s_add_i32 s57, 0, 0x14000
	v_mfma_f32_16x16x32_f16 v[114:117], v[26:29], v[14:17], 0
	s_waitcnt vmcnt(6)
	v_lshlrev_b32_e32 v133, 13, v154
	s_barrier
	v_mfma_f32_16x16x32_f16 v[106:109], v[26:29], v[10:13], 0
	v_mfma_f32_16x16x32_f16 v[78:81], v[142:145], v[14:17], 0
	v_mfma_f32_16x16x32_f16 v[74:77], v[138:141], v[14:17], 0
	v_mfma_f32_16x16x32_f16 v[70:73], v[142:145], v[10:13], 0
	v_mfma_f32_16x16x32_f16 v[66:69], v[138:141], v[10:13], 0
	v_mfma_f32_16x16x32_f16 v[58:61], v[26:29], v[22:25], 0
	v_mfma_f32_16x16x32_f16 v[50:53], v[26:29], v[18:21], 0
	v_mfma_f32_16x16x32_f16 v[42:45], v[26:29], v[134:137], 0
	v_mfma_f32_16x16x32_f16 v[34:37], v[142:145], v[22:25], 0
	v_mfma_f32_16x16x32_f16 v[26:29], v[138:141], v[22:25], 0
	v_mfma_f32_16x16x32_f16 v[22:25], v[142:145], v[18:21], 0
	v_mfma_f32_16x16x32_f16 v[18:21], v[138:141], v[18:21], 0
	v_mfma_f32_16x16x32_f16 v[14:17], v[142:145], v[134:137], 0
	v_mfma_f32_16x16x32_f16 v[10:13], v[138:141], v[134:137], 0
	v_add_u32_e32 v136, s57, v130
	v_add_u32_e32 v139, s82, v130
	v_add_u32_e32 v140, s83, v130
	v_or_b32_e32 v130, v151, v152
	v_lshlrev_b32_e32 v134, 6, v130
	s_movk_i32 s57, 0x3c0
	v_lshlrev_b32_e32 v130, 2, v130
	v_and_or_b32 v134, v134, s57, v146
	v_and_b32_e32 v130, 32, v130
	v_xad_u32 v130, v134, v130, 0
	v_or_b32_e32 v134, 16, v151
	v_or_b32_e32 v137, v134, v152
	v_lshlrev_b32_e32 v138, 6, v137
	v_lshlrev_b32_e32 v137, 2, v137
	v_and_or_b32 v138, v138, s57, v146
	v_and_b32_e32 v137, 32, v137
	v_lshlrev_b32_e32 v141, 7, v134
	v_or_b32_e32 v134, 32, v151
	v_xad_u32 v137, v138, v137, 0
	v_or_b32_e32 v138, v134, v152
	v_lshlrev_b32_e32 v142, 6, v138
	v_lshlrev_b32_e32 v138, 2, v138
	v_and_or_b32 v142, v142, s57, v146
	v_and_b32_e32 v138, 32, v138
	v_lshlrev_b32_e32 v143, 7, v134
	v_or_b32_e32 v134, 48, v151
	v_xad_u32 v142, v142, v138, 0
	v_or_b32_e32 v138, v134, v152
	v_lshlrev_b32_e32 v144, 6, v138
	v_lshlrev_b32_e32 v138, 2, v138
	v_and_or_b32 v144, v144, s57, v146
	v_and_b32_e32 v138, 32, v138
	v_lshlrev_b32_e32 v135, 12, v153
	v_xad_u32 v144, v144, v138, 0
	v_lshlrev_b32_e32 v145, 7, v134
	s_mov_b32 s57, 0
	v_add_u32_e32 v138, v131, v135
	v_add_u32_e32 v134, v130, v133
	v_add_u32_e32 v133, v137, v141
	v_add_u32_e32 v131, v142, v143
	v_add_u32_e32 v130, v144, v145
	v_add_u32_e32 v137, v136, v135
	v_add_u32_e32 v136, v139, v135
	v_add_u32_e32 v135, v140, v135
	s_cmp_lg_u32 s100, 0
	s_cbranch_scc1 .Lg2p_loop
.LBB2_356:
	ds_read_b128 v[140:143], v138
	ds_read_b128 v[154:157], v138 offset:1024
	ds_read_b128 v[158:161], v138 offset:2048
	ds_read_b128 v[164:167], v138 offset:3072
	s_lshl_b32 vcc_hi, s57, 7
	s_add_u32 s58, s88, vcc_hi
	s_addc_u32 s59, s89, 0
	s_add_u32 s82, s58, 0x80
	s_addc_u32 s83, s59, 0
	s_add_i32 s59, s97, 0xc000
	v_lshl_add_u64 v[144:145], s[82:83], 0, v[162:163]
	s_add_u32 s82, s82, 0x20000
	s_mov_b32 m0, s59
	s_addc_u32 s83, s83, 0
	s_add_i32 s58, s97, 0xe000
	ds_read_b128 v[168:171], v134
	ds_read_b128 v[172:175], v134 offset:1024
	ds_read_b128 v[176:179], v133
	ds_read_b128 v[184:187], v133 offset:1024
	ds_read_b128 v[188:191], v131
	ds_read_b128 v[192:195], v131 offset:1024
	ds_read_b128 v[196:199], v130
	ds_read_b128 v[200:203], v130 offset:1024
	global_load_lds_dwordx4 v[144:145], off
	s_mov_b32 m0, s58
	v_lshl_add_u64 v[144:145], s[82:83], 0, v[162:163]
	global_load_lds_dwordx4 v[144:145], off
	s_waitcnt lgkmcnt(8)
	s_barrier
	s_setprio 1
	s_waitcnt lgkmcnt(0)
	v_mfma_f32_16x16x32_f16 v[102:105], v[140:143], v[168:171], v[102:105]
	v_mfma_f32_16x16x32_f16 v[98:101], v[158:161], v[168:171], v[98:101]
	v_mfma_f32_16x16x32_f16 v[126:129], v[140:143], v[176:179], v[126:129]
	v_mfma_f32_16x16x32_f16 v[122:125], v[158:161], v[176:179], v[122:125]
	v_mfma_f32_16x16x32_f16 v[118:121], v[140:143], v[188:191], v[118:121]
	v_mfma_f32_16x16x32_f16 v[114:117], v[158:161], v[188:191], v[114:117]
	v_mfma_f32_16x16x32_f16 v[110:113], v[140:143], v[196:199], v[110:113]
	v_mfma_f32_16x16x32_f16 v[106:109], v[158:161], v[196:199], v[106:109]
	v_mfma_f32_16x16x32_f16 v[102:105], v[154:157], v[172:175], v[102:105]
	v_mfma_f32_16x16x32_f16 v[98:101], v[164:167], v[172:175], v[98:101]
	v_mfma_f32_16x16x32_f16 v[126:129], v[154:157], v[184:187], v[126:129]
	v_mfma_f32_16x16x32_f16 v[122:125], v[164:167], v[184:187], v[122:125]
	v_mfma_f32_16x16x32_f16 v[118:121], v[154:157], v[192:195], v[118:121]
	v_mfma_f32_16x16x32_f16 v[114:117], v[164:167], v[192:195], v[114:117]
	v_mfma_f32_16x16x32_f16 v[110:113], v[154:157], v[200:203], v[110:113]
	v_mfma_f32_16x16x32_f16 v[106:109], v[164:167], v[200:203], v[106:109]
	s_setprio 0
	s_barrier
	s_add_i32 vcc_lo, s57, 2
	s_lshl_b32 s78, vcc_lo, 7
	s_add_u32 s82, s92, s78
	s_addc_u32 s83, s93, 0
	s_mov_b32 m0, s84
	v_lshl_add_u64 v[144:145], s[82:83], 0, v[162:163]
	s_add_u32 s82, s82, 0x20000
	s_addc_u32 s83, s83, 0
	ds_read_b128 v[204:207], v137
	ds_read_b128 v[208:211], v137 offset:1024
	ds_read_b128 v[212:215], v137 offset:2048
	ds_read_b128 v[216:219], v137 offset:3072
	global_load_lds_dwordx4 v[144:145], off
	s_mov_b32 m0, s94
	v_lshl_add_u64 v[144:145], s[82:83], 0, v[162:163]
	global_load_lds_dwordx4 v[144:145], off
	s_barrier
	s_setprio 1
	s_waitcnt lgkmcnt(0)
	v_mfma_f32_16x16x32_f16 v[94:97], v[204:207], v[168:171], v[94:97]
	v_mfma_f32_16x16x32_f16 v[90:93], v[212:215], v[168:171], v[90:93]
	v_mfma_f32_16x16x32_f16 v[86:89], v[204:207], v[176:179], v[86:89]
	v_mfma_f32_16x16x32_f16 v[82:85], v[212:215], v[176:179], v[82:85]
	v_mfma_f32_16x16x32_f16 v[78:81], v[204:207], v[188:191], v[78:81]
	v_mfma_f32_16x16x32_f16 v[74:77], v[212:215], v[188:191], v[74:77]
	v_mfma_f32_16x16x32_f16 v[70:73], v[204:207], v[196:199], v[70:73]
	v_mfma_f32_16x16x32_f16 v[66:69], v[212:215], v[196:199], v[66:69]
	v_mfma_f32_16x16x32_f16 v[94:97], v[208:211], v[172:175], v[94:97]
	v_mfma_f32_16x16x32_f16 v[90:93], v[216:219], v[172:175], v[90:93]
	v_mfma_f32_16x16x32_f16 v[86:89], v[208:211], v[184:187], v[86:89]
	v_mfma_f32_16x16x32_f16 v[82:85], v[216:219], v[184:187], v[82:85]
	v_mfma_f32_16x16x32_f16 v[78:81], v[208:211], v[192:195], v[78:81]
	v_mfma_f32_16x16x32_f16 v[74:77], v[216:219], v[192:195], v[74:77]
	v_mfma_f32_16x16x32_f16 v[70:73], v[208:211], v[200:203], v[70:73]
	v_mfma_f32_16x16x32_f16 v[66:69], v[216:219], v[200:203], v[66:69]
	s_setprio 0
	s_add_u32 s82, s90, s78
	s_addc_u32 s83, s91, 0
	s_mov_b32 m0, s97
	v_lshl_add_u64 v[144:145], s[82:83], 0, v[162:163]
	s_add_u32 s82, s82, 0x20000
	s_addc_u32 s83, s83, 0
	s_barrier
	ds_read_b128 v[168:171], v134 offset:16384
	ds_read_b128 v[172:175], v134 offset:17408
	ds_read_b128 v[176:179], v133 offset:16384
	ds_read_b128 v[184:187], v133 offset:17408
	ds_read_b128 v[188:191], v131 offset:16384
	ds_read_b128 v[192:195], v131 offset:17408
	ds_read_b128 v[196:199], v130 offset:16384
	ds_read_b128 v[200:203], v130 offset:17408
	global_load_lds_dwordx4 v[144:145], off
	s_mov_b32 m0, s99
	v_lshl_add_u64 v[144:145], s[82:83], 0, v[162:163]
	global_load_lds_dwordx4 v[144:145], off
	s_barrier
	s_setprio 1
	s_waitcnt lgkmcnt(0)
	v_mfma_f32_16x16x32_f16 v[62:65], v[140:143], v[168:171], v[62:65]
	v_mfma_f32_16x16x32_f16 v[58:61], v[158:161], v[168:171], v[58:61]
	v_mfma_f32_16x16x32_f16 v[54:57], v[140:143], v[176:179], v[54:57]
	v_mfma_f32_16x16x32_f16 v[50:53], v[158:161], v[176:179], v[50:53]
	v_mfma_f32_16x16x32_f16 v[46:49], v[140:143], v[188:191], v[46:49]
	v_mfma_f32_16x16x32_f16 v[42:45], v[158:161], v[188:191], v[42:45]
	v_mfma_f32_16x16x32_f16 v[38:41], v[140:143], v[196:199], v[38:41]
	v_mfma_f32_16x16x32_f16 v[30:33], v[158:161], v[196:199], v[30:33]
	v_mfma_f32_16x16x32_f16 v[62:65], v[154:157], v[172:175], v[62:65]
	v_mfma_f32_16x16x32_f16 v[58:61], v[164:167], v[172:175], v[58:61]
	v_mfma_f32_16x16x32_f16 v[54:57], v[154:157], v[184:187], v[54:57]
	v_mfma_f32_16x16x32_f16 v[50:53], v[164:167], v[184:187], v[50:53]
	v_mfma_f32_16x16x32_f16 v[46:49], v[154:157], v[192:195], v[46:49]
	v_mfma_f32_16x16x32_f16 v[42:45], v[164:167], v[192:195], v[42:45]
	v_mfma_f32_16x16x32_f16 v[38:41], v[154:157], v[200:203], v[38:41]
	v_mfma_f32_16x16x32_f16 v[30:33], v[164:167], v[200:203], v[30:33]
	s_setprio 0
	s_barrier
	s_add_u32 s82, s34, s78
	s_addc_u32 s83, s35, 0
	s_mov_b32 m0, s95
	v_lshl_add_u64 v[140:141], s[82:83], 0, v[162:163]
	s_add_u32 s82, s82, 0x20000
	s_addc_u32 s83, s83, 0
	global_load_lds_dwordx4 v[140:141], off
	s_mov_b32 m0, s33
	v_lshl_add_u64 v[140:141], s[82:83], 0, v[162:163]
	global_load_lds_dwordx4 v[140:141], off
	s_waitcnt vmcnt(6)
	s_barrier
	s_setprio 1
	v_mfma_f32_16x16x32_f16 v[34:37], v[204:207], v[168:171], v[34:37]
	v_mfma_f32_16x16x32_f16 v[26:29], v[212:215], v[168:171], v[26:29]
	v_mfma_f32_16x16x32_f16 v[22:25], v[204:207], v[176:179], v[22:25]
	v_mfma_f32_16x16x32_f16 v[18:21], v[212:215], v[176:179], v[18:21]
	v_mfma_f32_16x16x32_f16 v[14:17], v[204:207], v[188:191], v[14:17]
	v_mfma_f32_16x16x32_f16 v[10:13], v[212:215], v[188:191], v[10:13]
	v_mfma_f32_16x16x32_f16 v[6:9], v[204:207], v[196:199], v[6:9]
	v_mfma_f32_16x16x32_f16 v[2:5], v[212:215], v[196:199], v[2:5]
	v_mfma_f32_16x16x32_f16 v[34:37], v[208:211], v[172:175], v[34:37]
	v_mfma_f32_16x16x32_f16 v[26:29], v[216:219], v[172:175], v[26:29]
	v_mfma_f32_16x16x32_f16 v[22:25], v[208:211], v[184:187], v[22:25]
	v_mfma_f32_16x16x32_f16 v[18:21], v[216:219], v[184:187], v[18:21]
	v_mfma_f32_16x16x32_f16 v[14:17], v[208:211], v[192:195], v[14:17]
	v_mfma_f32_16x16x32_f16 v[10:13], v[216:219], v[192:195], v[10:13]
	v_mfma_f32_16x16x32_f16 v[6:9], v[208:211], v[200:203], v[6:9]
	v_mfma_f32_16x16x32_f16 v[2:5], v[216:219], v[200:203], v[2:5]
	s_setprio 0
	s_barrier
	ds_read_b128 v[140:143], v136
	ds_read_b128 v[154:157], v136 offset:1024
	ds_read_b128 v[158:161], v136 offset:2048
	ds_read_b128 v[164:167], v136 offset:3072
	s_add_u32 s82, s88, s78
	s_addc_u32 s83, s89, 0
	s_mov_b32 m0, s11
	v_lshl_add_u64 v[144:145], s[82:83], 0, v[162:163]
	s_add_u32 s82, s82, 0x20000
	s_addc_u32 s83, s83, 0
	ds_read_b128 v[168:171], v134 offset:32768
	ds_read_b128 v[172:175], v134 offset:33792
	ds_read_b128 v[176:179], v133 offset:32768
	ds_read_b128 v[184:187], v133 offset:33792
	ds_read_b128 v[188:191], v131 offset:32768
	ds_read_b128 v[192:195], v131 offset:33792
	ds_read_b128 v[196:199], v130 offset:32768
	ds_read_b128 v[200:203], v130 offset:33792
	global_load_lds_dwordx4 v[144:145], off
	s_mov_b32 m0, s56
	v_lshl_add_u64 v[144:145], s[82:83], 0, v[162:163]
	global_load_lds_dwordx4 v[144:145], off
	s_waitcnt lgkmcnt(8)
	s_barrier
	s_setprio 1
	s_waitcnt lgkmcnt(0)
	v_mfma_f32_16x16x32_f16 v[102:105], v[140:143], v[168:171], v[102:105]
	v_mfma_f32_16x16x32_f16 v[98:101], v[158:161], v[168:171], v[98:101]
	v_mfma_f32_16x16x32_f16 v[126:129], v[140:143], v[176:179], v[126:129]
	v_mfma_f32_16x16x32_f16 v[122:125], v[158:161], v[176:179], v[122:125]
	v_mfma_f32_16x16x32_f16 v[118:121], v[140:143], v[188:191], v[118:121]
	v_mfma_f32_16x16x32_f16 v[114:117], v[158:161], v[188:191], v[114:117]
	v_mfma_f32_16x16x32_f16 v[110:113], v[140:143], v[196:199], v[110:113]
	v_mfma_f32_16x16x32_f16 v[106:109], v[158:161], v[196:199], v[106:109]
	v_mfma_f32_16x16x32_f16 v[102:105], v[154:157], v[172:175], v[102:105]
	v_mfma_f32_16x16x32_f16 v[98:101], v[164:167], v[172:175], v[98:101]
	v_mfma_f32_16x16x32_f16 v[126:129], v[154:157], v[184:187], v[126:129]
	v_mfma_f32_16x16x32_f16 v[122:125], v[164:167], v[184:187], v[122:125]
	v_mfma_f32_16x16x32_f16 v[118:121], v[154:157], v[192:195], v[118:121]
	v_mfma_f32_16x16x32_f16 v[114:117], v[164:167], v[192:195], v[114:117]
	v_mfma_f32_16x16x32_f16 v[110:113], v[154:157], v[200:203], v[110:113]
	v_mfma_f32_16x16x32_f16 v[106:109], v[164:167], v[200:203], v[106:109]
	s_setprio 0
	s_barrier
	s_add_u32 s78, s92, vcc_hi
	s_addc_u32 s79, s93, 0
	s_add_u32 s82, s78, 0x180
	s_addc_u32 s83, s79, 0
	s_add_i32 m0, s97, 0x18000
	v_lshl_add_u64 v[144:145], s[82:83], 0, v[162:163]
	s_add_u32 s82, s82, 0x20000
	s_addc_u32 s83, s83, 0
	ds_read_b128 v[204:207], v135
	ds_read_b128 v[208:211], v135 offset:1024
	ds_read_b128 v[212:215], v135 offset:2048
	ds_read_b128 v[216:219], v135 offset:3072
	global_load_lds_dwordx4 v[144:145], off
	s_add_i32 m0, s97, 0x1a000
	v_lshl_add_u64 v[144:145], s[82:83], 0, v[162:163]
	global_load_lds_dwordx4 v[144:145], off
	s_barrier
	s_setprio 1
	s_waitcnt lgkmcnt(0)
	v_mfma_f32_16x16x32_f16 v[94:97], v[204:207], v[168:171], v[94:97]
	v_mfma_f32_16x16x32_f16 v[90:93], v[212:215], v[168:171], v[90:93]
	v_mfma_f32_16x16x32_f16 v[86:89], v[204:207], v[176:179], v[86:89]
	v_mfma_f32_16x16x32_f16 v[82:85], v[212:215], v[176:179], v[82:85]
	v_mfma_f32_16x16x32_f16 v[78:81], v[204:207], v[188:191], v[78:81]
	v_mfma_f32_16x16x32_f16 v[74:77], v[212:215], v[188:191], v[74:77]
	v_mfma_f32_16x16x32_f16 v[70:73], v[204:207], v[196:199], v[70:73]
	v_mfma_f32_16x16x32_f16 v[66:69], v[212:215], v[196:199], v[66:69]
	v_mfma_f32_16x16x32_f16 v[94:97], v[208:211], v[172:175], v[94:97]
	v_mfma_f32_16x16x32_f16 v[90:93], v[216:219], v[172:175], v[90:93]
	v_mfma_f32_16x16x32_f16 v[86:89], v[208:211], v[184:187], v[86:89]
	v_mfma_f32_16x16x32_f16 v[82:85], v[216:219], v[184:187], v[82:85]
	v_mfma_f32_16x16x32_f16 v[78:81], v[208:211], v[192:195], v[78:81]
	v_mfma_f32_16x16x32_f16 v[74:77], v[216:219], v[192:195], v[74:77]
	v_mfma_f32_16x16x32_f16 v[70:73], v[208:211], v[200:203], v[70:73]
	v_mfma_f32_16x16x32_f16 v[66:69], v[216:219], v[200:203], v[66:69]
	s_setprio 0
	s_add_u32 s78, s90, vcc_hi
	s_addc_u32 s79, s91, 0
	s_add_u32 s82, s78, 0x180
	s_addc_u32 s83, s79, 0
	s_mov_b32 m0, s52
	v_lshl_add_u64 v[144:145], s[82:83], 0, v[162:163]
	s_add_u32 s82, s82, 0x20000
	s_addc_u32 s83, s83, 0
	s_barrier
	ds_read_b128 v[168:171], v134 offset:49152
	ds_read_b128 v[172:175], v134 offset:50176
	ds_read_b128 v[176:179], v133 offset:49152
	ds_read_b128 v[184:187], v133 offset:50176
	ds_read_b128 v[188:191], v131 offset:49152
	ds_read_b128 v[192:195], v131 offset:50176
	ds_read_b128 v[196:199], v130 offset:49152
	ds_read_b128 v[200:203], v130 offset:50176
	global_load_lds_dwordx4 v[144:145], off
	s_mov_b32 m0, s53
	v_lshl_add_u64 v[144:145], s[82:83], 0, v[162:163]
	global_load_lds_dwordx4 v[144:145], off
	s_barrier
	s_setprio 1
	s_waitcnt lgkmcnt(0)
	v_mfma_f32_16x16x32_f16 v[62:65], v[140:143], v[168:171], v[62:65]
	v_mfma_f32_16x16x32_f16 v[58:61], v[158:161], v[168:171], v[58:61]
	v_mfma_f32_16x16x32_f16 v[54:57], v[140:143], v[176:179], v[54:57]
	v_mfma_f32_16x16x32_f16 v[50:53], v[158:161], v[176:179], v[50:53]
	v_mfma_f32_16x16x32_f16 v[46:49], v[140:143], v[188:191], v[46:49]
	v_mfma_f32_16x16x32_f16 v[42:45], v[158:161], v[188:191], v[42:45]
	v_mfma_f32_16x16x32_f16 v[38:41], v[140:143], v[196:199], v[38:41]
	v_mfma_f32_16x16x32_f16 v[30:33], v[158:161], v[196:199], v[30:33]
	v_mfma_f32_16x16x32_f16 v[62:65], v[154:157], v[172:175], v[62:65]
	v_mfma_f32_16x16x32_f16 v[58:61], v[164:167], v[172:175], v[58:61]
	v_mfma_f32_16x16x32_f16 v[54:57], v[154:157], v[184:187], v[54:57]
	v_mfma_f32_16x16x32_f16 v[50:53], v[164:167], v[184:187], v[50:53]
	v_mfma_f32_16x16x32_f16 v[46:49], v[154:157], v[192:195], v[46:49]
	v_mfma_f32_16x16x32_f16 v[42:45], v[164:167], v[192:195], v[42:45]
	v_mfma_f32_16x16x32_f16 v[38:41], v[154:157], v[200:203], v[38:41]
	v_mfma_f32_16x16x32_f16 v[30:33], v[164:167], v[200:203], v[30:33]
	s_setprio 0
	s_barrier
	s_add_u32 s78, s34, vcc_hi
	s_addc_u32 s79, s35, 0
	s_add_u32 s82, s78, 0x180
	s_addc_u32 s83, s79, 0
	s_add_i32 m0, s97, 0x1c000
	v_lshl_add_u64 v[140:141], s[82:83], 0, v[162:163]
	s_add_u32 s82, s82, 0x20000
	s_addc_u32 s83, s83, 0
	global_load_lds_dwordx4 v[140:141], off
	s_add_i32 m0, s97, 0x1e000
	v_lshl_add_u64 v[140:141], s[82:83], 0, v[162:163]
	global_load_lds_dwordx4 v[140:141], off
	s_waitcnt vmcnt(6)
	s_barrier
	s_setprio 1
	v_mfma_f32_16x16x32_f16 v[34:37], v[204:207], v[168:171], v[34:37]
	v_mfma_f32_16x16x32_f16 v[26:29], v[212:215], v[168:171], v[26:29]
	v_mfma_f32_16x16x32_f16 v[22:25], v[204:207], v[176:179], v[22:25]
	v_mfma_f32_16x16x32_f16 v[18:21], v[212:215], v[176:179], v[18:21]
	v_mfma_f32_16x16x32_f16 v[14:17], v[204:207], v[188:191], v[14:17]
	v_mfma_f32_16x16x32_f16 v[10:13], v[212:215], v[188:191], v[10:13]
	v_mfma_f32_16x16x32_f16 v[6:9], v[204:207], v[196:199], v[6:9]
	v_mfma_f32_16x16x32_f16 v[2:5], v[212:215], v[196:199], v[2:5]
	v_mfma_f32_16x16x32_f16 v[34:37], v[208:211], v[172:175], v[34:37]
	v_mfma_f32_16x16x32_f16 v[26:29], v[216:219], v[172:175], v[26:29]
	v_mfma_f32_16x16x32_f16 v[22:25], v[208:211], v[184:187], v[22:25]
	v_mfma_f32_16x16x32_f16 v[18:21], v[216:219], v[184:187], v[18:21]
	v_mfma_f32_16x16x32_f16 v[14:17], v[208:211], v[192:195], v[14:17]
	v_mfma_f32_16x16x32_f16 v[10:13], v[216:219], v[192:195], v[10:13]
	v_mfma_f32_16x16x32_f16 v[6:9], v[208:211], v[200:203], v[6:9]
	v_mfma_f32_16x16x32_f16 v[2:5], v[216:219], v[200:203], v[2:5]
	s_setprio 0
	s_cmp_lt_u32 s57, 12
	s_mov_b32 s57, vcc_lo
	s_barrier
	s_cbranch_scc1 .LBB2_356
	s_add_u32 s34, s88, 0x780
	s_addc_u32 s35, s89, 0
	ds_read_b128 v[140:143], v138
	ds_read_b128 v[154:157], v138 offset:1024
	ds_read_b128 v[158:161], v138 offset:2048
	ds_read_b128 v[164:167], v138 offset:3072
	ds_read_b128 v[168:171], v134
	ds_read_b128 v[172:175], v134 offset:1024
	ds_read_b128 v[176:179], v133
	ds_read_b128 v[184:187], v133 offset:1024
	ds_read_b128 v[188:191], v131
	ds_read_b128 v[192:195], v131 offset:1024
	ds_read_b128 v[196:199], v130
	ds_read_b128 v[200:203], v130 offset:1024
	v_lshl_add_u64 v[138:139], s[34:35], 0, v[162:163]
	s_add_u32 s34, s34, 0x20000
	s_mov_b32 m0, s59
	s_addc_u32 s35, s35, 0
	global_load_lds_dwordx4 v[138:139], off
	s_mov_b32 m0, s58
	v_lshl_add_u64 v[138:139], s[34:35], 0, v[162:163]
	global_load_lds_dwordx4 v[138:139], off
	s_barrier
	s_setprio 1
	s_waitcnt lgkmcnt(0)
	v_mfma_f32_16x16x32_f16 v[102:105], v[140:143], v[168:171], v[102:105]
	v_mfma_f32_16x16x32_f16 v[98:101], v[158:161], v[168:171], v[98:101]
	v_mfma_f32_16x16x32_f16 v[126:129], v[140:143], v[176:179], v[126:129]
	v_mfma_f32_16x16x32_f16 v[122:125], v[158:161], v[176:179], v[122:125]
	v_mfma_f32_16x16x32_f16 v[118:121], v[140:143], v[188:191], v[118:121]
	v_mfma_f32_16x16x32_f16 v[114:117], v[158:161], v[188:191], v[114:117]
	v_mfma_f32_16x16x32_f16 v[110:113], v[140:143], v[196:199], v[110:113]
	v_mfma_f32_16x16x32_f16 v[106:109], v[158:161], v[196:199], v[106:109]
	v_mfma_f32_16x16x32_f16 v[102:105], v[154:157], v[172:175], v[102:105]
	v_mfma_f32_16x16x32_f16 v[98:101], v[164:167], v[172:175], v[98:101]
	v_mfma_f32_16x16x32_f16 v[126:129], v[154:157], v[184:187], v[126:129]
	v_mfma_f32_16x16x32_f16 v[122:125], v[164:167], v[184:187], v[122:125]
	v_mfma_f32_16x16x32_f16 v[118:121], v[154:157], v[192:195], v[118:121]
	v_mfma_f32_16x16x32_f16 v[114:117], v[164:167], v[192:195], v[114:117]
	v_mfma_f32_16x16x32_f16 v[110:113], v[154:157], v[200:203], v[110:113]
	v_mfma_f32_16x16x32_f16 v[106:109], v[164:167], v[200:203], v[106:109]
	s_setprio 0
	s_barrier
	ds_read_b128 v[204:207], v137
	ds_read_b128 v[208:211], v137 offset:1024
	ds_read_b128 v[212:215], v137 offset:2048
	ds_read_b128 v[216:219], v137 offset:3072
	s_barrier
	s_setprio 1
	s_waitcnt lgkmcnt(0)
	v_mfma_f32_16x16x32_f16 v[94:97], v[204:207], v[168:171], v[94:97]
	v_mfma_f32_16x16x32_f16 v[94:97], v[208:211], v[172:175], v[94:97]
	v_mfma_f32_16x16x32_f16 v[90:93], v[212:215], v[168:171], v[90:93]
	v_mfma_f32_16x16x32_f16 v[86:89], v[204:207], v[176:179], v[86:89]
	v_mfma_f32_16x16x32_f16 v[82:85], v[212:215], v[176:179], v[82:85]
	v_mfma_f32_16x16x32_f16 v[78:81], v[204:207], v[188:191], v[78:81]
	v_mfma_f32_16x16x32_f16 v[74:77], v[212:215], v[188:191], v[74:77]
	v_mfma_f32_16x16x32_f16 v[70:73], v[204:207], v[196:199], v[70:73]
	v_mfma_f32_16x16x32_f16 v[66:69], v[212:215], v[196:199], v[66:69]
	v_mfma_f32_16x16x32_f16 v[168:171], v[216:219], v[172:175], v[90:93]
	v_mfma_f32_16x16x32_f16 v[172:175], v[208:211], v[184:187], v[86:89]
	v_mfma_f32_16x16x32_f16 v[176:179], v[216:219], v[184:187], v[82:85]
	v_mfma_f32_16x16x32_f16 v[184:187], v[208:211], v[192:195], v[78:81]
	v_mfma_f32_16x16x32_f16 v[188:191], v[216:219], v[192:195], v[74:77]
	v_mfma_f32_16x16x32_f16 v[192:195], v[208:211], v[200:203], v[70:73]
	v_mfma_f32_16x16x32_f16 v[196:199], v[216:219], v[200:203], v[66:69]
	s_setprio 0
	s_barrier
	s_nop 0
	ds_read_b128 v[66:69], v134 offset:16384
	ds_read_b128 v[70:73], v134 offset:17408
	ds_read_b128 v[74:77], v133 offset:16384
	ds_read_b128 v[78:81], v133 offset:17408
	ds_read_b128 v[82:85], v131 offset:16384
	ds_read_b128 v[86:89], v131 offset:17408
	ds_read_b128 v[90:93], v130 offset:16384
	ds_read_b128 v[200:203], v130 offset:17408
	s_waitcnt vmcnt(4)
	s_barrier
	s_setprio 1
	s_waitcnt lgkmcnt(0)
	v_mfma_f32_16x16x32_f16 v[62:65], v[140:143], v[66:69], v[62:65]
	v_mfma_f32_16x16x32_f16 v[58:61], v[158:161], v[66:69], v[58:61]
	v_mfma_f32_16x16x32_f16 v[54:57], v[140:143], v[74:77], v[54:57]
	v_mfma_f32_16x16x32_f16 v[50:53], v[158:161], v[74:77], v[50:53]
	v_mfma_f32_16x16x32_f16 v[46:49], v[140:143], v[82:85], v[46:49]
	v_mfma_f32_16x16x32_f16 v[42:45], v[158:161], v[82:85], v[42:45]
	v_mfma_f32_16x16x32_f16 v[38:41], v[140:143], v[90:93], v[38:41]
	v_mfma_f32_16x16x32_f16 v[62:65], v[154:157], v[70:73], v[62:65]
	v_mfma_f32_16x16x32_f16 v[58:61], v[164:167], v[70:73], v[58:61]
	v_mfma_f32_16x16x32_f16 v[54:57], v[154:157], v[78:81], v[54:57]
	v_mfma_f32_16x16x32_f16 v[50:53], v[164:167], v[78:81], v[50:53]
	v_mfma_f32_16x16x32_f16 v[46:49], v[154:157], v[86:89], v[46:49]
	v_mfma_f32_16x16x32_f16 v[42:45], v[164:167], v[86:89], v[42:45]
	v_mfma_f32_16x16x32_f16 v[38:41], v[154:157], v[200:203], v[38:41]
	v_mfma_f32_16x16x32_f16 v[30:33], v[158:161], v[90:93], v[30:33]
	v_mfma_f32_16x16x32_f16 v[138:141], v[164:167], v[200:203], v[30:33]
	s_setprio 0
	s_setprio 1
	v_mfma_f32_16x16x32_f16 v[30:33], v[204:207], v[66:69], v[34:37]
	v_mfma_f32_16x16x32_f16 v[34:37], v[208:211], v[70:73], v[30:33]
	v_mfma_f32_16x16x32_f16 v[26:29], v[212:215], v[66:69], v[26:29]
	v_mfma_f32_16x16x32_f16 v[22:25], v[204:207], v[74:77], v[22:25]
	v_mfma_f32_16x16x32_f16 v[18:21], v[212:215], v[74:77], v[18:21]
	v_mfma_f32_16x16x32_f16 v[14:17], v[204:207], v[82:85], v[14:17]
	v_mfma_f32_16x16x32_f16 v[10:13], v[212:215], v[82:85], v[10:13]
	v_mfma_f32_16x16x32_f16 v[6:9], v[204:207], v[90:93], v[6:9]
	v_mfma_f32_16x16x32_f16 v[2:5], v[212:215], v[90:93], v[2:5]
	v_mfma_f32_16x16x32_f16 v[142:145], v[216:219], v[70:73], v[26:29]
	v_mfma_f32_16x16x32_f16 v[154:157], v[208:211], v[78:81], v[22:25]
	v_mfma_f32_16x16x32_f16 v[158:161], v[216:219], v[78:81], v[18:21]
	v_mfma_f32_16x16x32_f16 v[164:167], v[208:211], v[86:89], v[14:17]
	v_mfma_f32_16x16x32_f16 v[220:223], v[216:219], v[86:89], v[10:13]
	v_mfma_f32_16x16x32_f16 v[204:207], v[208:211], v[200:203], v[6:9]
	v_mfma_f32_16x16x32_f16 v[200:203], v[216:219], v[200:203], v[2:5]
	s_setprio 0
	s_barrier
	s_nop 0
	ds_read_b128 v[2:5], v136
	ds_read_b128 v[6:9], v136 offset:1024
	ds_read_b128 v[208:211], v136 offset:2048
	ds_read_b128 v[212:215], v136 offset:3072
	ds_read_b128 v[10:13], v134 offset:32768
	ds_read_b128 v[14:17], v134 offset:33792
	ds_read_b128 v[18:21], v133 offset:32768
	ds_read_b128 v[22:25], v133 offset:33792
	ds_read_b128 v[26:29], v131 offset:32768
	ds_read_b128 v[30:33], v131 offset:33792
	ds_read_b128 v[216:219], v130 offset:32768
	ds_read_b128 v[224:227], v130 offset:33792
	s_waitcnt vmcnt(2)
	s_barrier
	s_setprio 1
	s_waitcnt lgkmcnt(0)
	v_mfma_f32_16x16x32_f16 v[66:69], v[2:5], v[10:13], v[102:105]
	v_mfma_f32_16x16x32_f16 v[90:93], v[6:9], v[14:17], v[66:69]
	v_mfma_f32_16x16x32_f16 v[66:69], v[208:211], v[10:13], v[98:101]
	v_mfma_f32_16x16x32_f16 v[98:101], v[212:215], v[14:17], v[66:69]
	v_mfma_f32_16x16x32_f16 v[66:69], v[2:5], v[18:21], v[126:129]
	v_mfma_f32_16x16x32_f16 v[82:85], v[6:9], v[22:25], v[66:69]
	v_mfma_f32_16x16x32_f16 v[66:69], v[208:211], v[18:21], v[122:125]
	v_mfma_f32_16x16x32_f16 v[86:89], v[212:215], v[22:25], v[66:69]
	v_mfma_f32_16x16x32_f16 v[66:69], v[2:5], v[26:29], v[118:121]
	v_mfma_f32_16x16x32_f16 v[74:77], v[6:9], v[30:33], v[66:69]
	v_mfma_f32_16x16x32_f16 v[66:69], v[208:211], v[26:29], v[114:117]
	v_mfma_f32_16x16x32_f16 v[78:81], v[212:215], v[30:33], v[66:69]
	v_mfma_f32_16x16x32_f16 v[66:69], v[2:5], v[216:219], v[110:113]
	v_mfma_f32_16x16x32_f16 v[70:73], v[208:211], v[216:219], v[106:109]
	v_mfma_f32_16x16x32_f16 v[66:69], v[6:9], v[224:227], v[66:69]
	v_mfma_f32_16x16x32_f16 v[70:73], v[212:215], v[224:227], v[70:73]
	s_setprio 0
	s_barrier
	ds_read_b128 v[228:231], v135
	ds_read_b128 v[232:235], v135 offset:1024
	ds_read_b128 v[236:239], v135 offset:2048
	ds_read_b128 v[240:243], v135 offset:3072
	s_waitcnt vmcnt(0)
	s_barrier
	s_setprio 1
	s_waitcnt lgkmcnt(0)
	v_mfma_f32_16x16x32_f16 v[94:97], v[228:231], v[10:13], v[94:97]
	v_mfma_f32_16x16x32_f16 v[10:13], v[236:239], v[10:13], v[168:171]
	v_mfma_f32_16x16x32_f16 v[126:129], v[240:243], v[14:17], v[10:13]
	v_mfma_f32_16x16x32_f16 v[10:13], v[228:231], v[18:21], v[172:175]
	v_mfma_f32_16x16x32_f16 v[114:117], v[232:235], v[22:25], v[10:13]
	v_mfma_f32_16x16x32_f16 v[10:13], v[236:239], v[18:21], v[176:179]
	v_mfma_f32_16x16x32_f16 v[118:121], v[240:243], v[22:25], v[10:13]
	v_mfma_f32_16x16x32_f16 v[10:13], v[228:231], v[26:29], v[184:187]
	v_mfma_f32_16x16x32_f16 v[106:109], v[232:235], v[30:33], v[10:13]
	v_mfma_f32_16x16x32_f16 v[10:13], v[236:239], v[26:29], v[188:191]
	v_mfma_f32_16x16x32_f16 v[110:113], v[240:243], v[30:33], v[10:13]
	v_mfma_f32_16x16x32_f16 v[10:13], v[228:231], v[216:219], v[192:195]
	v_mfma_f32_16x16x32_f16 v[122:125], v[232:235], v[14:17], v[94:97]
	v_mfma_f32_16x16x32_f16 v[94:97], v[232:235], v[224:227], v[10:13]
	v_mfma_f32_16x16x32_f16 v[10:13], v[236:239], v[216:219], v[196:199]
	v_mfma_f32_16x16x32_f16 v[102:105], v[240:243], v[224:227], v[10:13]
	s_setprio 0
	s_barrier
	ds_read_b128 v[168:171], v134 offset:49152
	ds_read_b128 v[134:137], v134 offset:50176
	ds_read_b128 v[172:175], v133 offset:49152
	ds_read_b128 v[176:179], v133 offset:50176
	ds_read_b128 v[184:187], v131 offset:49152
	ds_read_b128 v[188:191], v131 offset:50176
	ds_read_b128 v[192:195], v130 offset:49152
	ds_read_b128 v[196:199], v130 offset:50176
	s_barrier
	s_setprio 1
	s_waitcnt lgkmcnt(0)
	v_mfma_f32_16x16x32_f16 v[10:13], v[2:5], v[168:171], v[62:65]
	v_mfma_f32_16x16x32_f16 v[26:29], v[6:9], v[134:137], v[10:13]
	v_mfma_f32_16x16x32_f16 v[10:13], v[208:211], v[168:171], v[58:61]
	v_mfma_f32_16x16x32_f16 v[30:33], v[212:215], v[134:137], v[10:13]
	v_mfma_f32_16x16x32_f16 v[10:13], v[2:5], v[172:175], v[54:57]
	v_mfma_f32_16x16x32_f16 v[18:21], v[6:9], v[176:179], v[10:13]
	v_mfma_f32_16x16x32_f16 v[10:13], v[208:211], v[172:175], v[50:53]
	v_mfma_f32_16x16x32_f16 v[22:25], v[212:215], v[176:179], v[10:13]
	v_mfma_f32_16x16x32_f16 v[10:13], v[2:5], v[184:187], v[46:49]
	v_mfma_f32_16x16x32_f16 v[2:5], v[2:5], v[192:195], v[38:41]
	v_mfma_f32_16x16x32_f16 v[10:13], v[6:9], v[188:191], v[10:13]
	v_mfma_f32_16x16x32_f16 v[14:17], v[208:211], v[184:187], v[42:45]
	v_mfma_f32_16x16x32_f16 v[2:5], v[6:9], v[196:199], v[2:5]
	v_mfma_f32_16x16x32_f16 v[6:9], v[208:211], v[192:195], v[138:141]
	v_mfma_f32_16x16x32_f16 v[14:17], v[212:215], v[188:191], v[14:17]
	v_mfma_f32_16x16x32_f16 v[6:9], v[212:215], v[196:199], v[6:9]
	s_setprio 0
	s_setprio 1
	v_mfma_f32_16x16x32_f16 v[34:37], v[228:231], v[168:171], v[34:37]
	v_mfma_f32_16x16x32_f16 v[58:61], v[232:235], v[134:137], v[34:37]
	v_mfma_f32_16x16x32_f16 v[34:37], v[236:239], v[168:171], v[142:145]
	v_mfma_f32_16x16x32_f16 v[62:65], v[240:243], v[134:137], v[34:37]
	v_mfma_f32_16x16x32_f16 v[34:37], v[228:231], v[172:175], v[154:157]
	v_mfma_f32_16x16x32_f16 v[50:53], v[232:235], v[176:179], v[34:37]
	v_mfma_f32_16x16x32_f16 v[34:37], v[236:239], v[172:175], v[158:161]
	v_mfma_f32_16x16x32_f16 v[54:57], v[240:243], v[176:179], v[34:37]
	v_mfma_f32_16x16x32_f16 v[34:37], v[228:231], v[184:187], v[164:167]
	v_mfma_f32_16x16x32_f16 v[42:45], v[232:235], v[188:191], v[34:37]
	v_mfma_f32_16x16x32_f16 v[34:37], v[236:239], v[184:187], v[220:223]
	v_mfma_f32_16x16x32_f16 v[46:49], v[240:243], v[188:191], v[34:37]
	v_mfma_f32_16x16x32_f16 v[34:37], v[228:231], v[192:195], v[204:207]
	v_mfma_f32_16x16x32_f16 v[38:41], v[236:239], v[192:195], v[200:203]
	v_mfma_f32_16x16x32_f16 v[34:37], v[232:235], v[196:199], v[34:37]
	v_mfma_f32_16x16x32_f16 v[38:41], v[240:243], v[196:199], v[38:41]
	s_setprio 0

.LBB2_359:
	s_or_b64 exec, exec, s[34:35]
	s_mov_b64 s[78:79], s[80:81]
	v_lshrrev_b32_e32 v156, 2, v149
	v_lshl_add_u32 v156, v156, 6, v152
	v_lshlrev_b32_e32 v157, 2, v156
	v_add_u32_e32 v157, 0x20000, v157
	ds_read_b32 v164, v157 offset:0
	ds_read_b32 v166, v157 offset:64
	ds_read_b32 v168, v157 offset:128
	ds_read_b32 v170, v157 offset:192
	ds_read_b32 v172, v157 offset:512
	ds_read_b32 v174, v157 offset:576
	ds_read_b32 v176, v157 offset:640
	ds_read_b32 v178, v157 offset:704
	v_lshrrev_b32_e32 v158, 1, v156
	v_and_b32_e32 v158, 7, v158
	v_lshlrev_b32_e32 v158, 4, v158
	v_lshlrev_b32_e32 v159, 6, v153
	v_lshl_add_u32 v159, v147, 3, v159
	v_xor_b32_e32 v159, v159, v158
	v_lshl_add_u32 v184, v156, 9, v159
	v_xor_b32_e32 v185, 32, v184
	v_add_u32_e32 v186, 0x10000, v184
	v_add_u32_e32 v187, 0x10000, v185
	v_lshrrev_b32_e32 v196, 5, v150
	v_lshl_add_u32 v196, v149, 5, v196
	v_and_b32_e32 v197, 31, v150
	v_lshlrev_b32_e32 v197, 4, v197
	s_lshl_b32 s34, s98, 12
	s_lshl_b32 s35, s87, 1
	s_add_u32 s34, s34, s35
	v_lshl_add_u32 v208, v196, 12, v197
	v_add_u32_e32 v208, s34, v208
	v_lshlrev_b32_e32 v196, 9, v196
	v_xor_b32_e32 v200, 0, v197
	v_xor_b32_e32 v201, 16, v197
	v_xor_b32_e32 v202, 32, v197
	v_xor_b32_e32 v203, 48, v197
	v_xor_b32_e32 v204, 64, v197
	v_xor_b32_e32 v205, 80, v197
	v_xor_b32_e32 v206, 96, v197
	v_xor_b32_e32 v207, 112, v197
	v_add_u32_e32 v200, v200, v196
	v_add_u32_e32 v201, v201, v196
	v_add_u32_e32 v202, v202, v196
	v_add_u32_e32 v203, v203, v196
	v_add_u32_e32 v204, v204, v196
	v_add_u32_e32 v205, v205, v196
	v_add_u32_e32 v206, v206, v196
	v_add_u32_e32 v207, v207, v196
	s_waitcnt lgkmcnt(0)
	v_pk_mul_f32 v[90:91], v[90:91], v[164:165] op_sel_hi:[1,0]
	v_pk_mul_f32 v[92:93], v[92:93], v[164:165] op_sel_hi:[1,0]
	v_cvt_pk_f16_f32 v188, v90, v91
	v_cvt_pk_f16_f32 v189, v92, v93
	ds_write_b64 v184, v[188:189]
	v_pk_mul_f32 v[98:99], v[98:99], v[164:165] op_sel_hi:[1,0]
	v_pk_mul_f32 v[100:101], v[100:101], v[164:165] op_sel_hi:[1,0]
	v_cvt_pk_f16_f32 v190, v98, v99
	v_cvt_pk_f16_f32 v191, v100, v101
	ds_write_b64 v185, v[190:191]
	v_pk_mul_f32 v[122:123], v[122:123], v[164:165] op_sel_hi:[1,0]
	v_pk_mul_f32 v[124:125], v[124:125], v[164:165] op_sel_hi:[1,0]
	v_cvt_pk_f16_f32 v192, v122, v123
	v_cvt_pk_f16_f32 v193, v124, v125
	ds_write_b64 v184, v[192:193] offset:256
	v_pk_mul_f32 v[126:127], v[126:127], v[164:165] op_sel_hi:[1,0]
	v_pk_mul_f32 v[128:129], v[128:129], v[164:165] op_sel_hi:[1,0]
	v_cvt_pk_f16_f32 v194, v126, v127
	v_cvt_pk_f16_f32 v195, v128, v129
	ds_write_b64 v185, v[194:195] offset:256
	v_pk_mul_f32 v[82:83], v[82:83], v[166:167] op_sel_hi:[1,0]
	v_pk_mul_f32 v[84:85], v[84:85], v[166:167] op_sel_hi:[1,0]
	v_cvt_pk_f16_f32 v188, v82, v83
	v_cvt_pk_f16_f32 v189, v84, v85
	ds_write_b64 v184, v[188:189] offset:8192
	v_pk_mul_f32 v[86:87], v[86:87], v[166:167] op_sel_hi:[1,0]
	v_pk_mul_f32 v[88:89], v[88:89], v[166:167] op_sel_hi:[1,0]
	v_cvt_pk_f16_f32 v190, v86, v87
	v_cvt_pk_f16_f32 v191, v88, v89
	ds_write_b64 v185, v[190:191] offset:8192
	v_pk_mul_f32 v[114:115], v[114:115], v[166:167] op_sel_hi:[1,0]
	v_pk_mul_f32 v[116:117], v[116:117], v[166:167] op_sel_hi:[1,0]
	v_cvt_pk_f16_f32 v192, v114, v115
	v_cvt_pk_f16_f32 v193, v116, v117
	ds_write_b64 v184, v[192:193] offset:8448
	v_pk_mul_f32 v[118:119], v[118:119], v[166:167] op_sel_hi:[1,0]
	v_pk_mul_f32 v[120:121], v[120:121], v[166:167] op_sel_hi:[1,0]
	v_cvt_pk_f16_f32 v194, v118, v119
	v_cvt_pk_f16_f32 v195, v120, v121
	ds_write_b64 v185, v[194:195] offset:8448
	v_pk_mul_f32 v[74:75], v[74:75], v[168:169] op_sel_hi:[1,0]
	v_pk_mul_f32 v[76:77], v[76:77], v[168:169] op_sel_hi:[1,0]
	v_cvt_pk_f16_f32 v188, v74, v75
	v_cvt_pk_f16_f32 v189, v76, v77
	ds_write_b64 v184, v[188:189] offset:16384
	v_pk_mul_f32 v[78:79], v[78:79], v[168:169] op_sel_hi:[1,0]
	v_pk_mul_f32 v[80:81], v[80:81], v[168:169] op_sel_hi:[1,0]
	v_cvt_pk_f16_f32 v190, v78, v79
	v_cvt_pk_f16_f32 v191, v80, v81
	ds_write_b64 v185, v[190:191] offset:16384
	v_pk_mul_f32 v[106:107], v[106:107], v[168:169] op_sel_hi:[1,0]
	v_pk_mul_f32 v[108:109], v[108:109], v[168:169] op_sel_hi:[1,0]
	v_cvt_pk_f16_f32 v192, v106, v107
	v_cvt_pk_f16_f32 v193, v108, v109
	ds_write_b64 v184, v[192:193] offset:16640
	v_pk_mul_f32 v[110:111], v[110:111], v[168:169] op_sel_hi:[1,0]
	v_pk_mul_f32 v[112:113], v[112:113], v[168:169] op_sel_hi:[1,0]
	v_cvt_pk_f16_f32 v194, v110, v111
	v_cvt_pk_f16_f32 v195, v112, v113
	ds_write_b64 v185, v[194:195] offset:16640
	v_pk_mul_f32 v[66:67], v[66:67], v[170:171] op_sel_hi:[1,0]
	v_pk_mul_f32 v[68:69], v[68:69], v[170:171] op_sel_hi:[1,0]
	v_cvt_pk_f16_f32 v188, v66, v67
	v_cvt_pk_f16_f32 v189, v68, v69
	ds_write_b64 v184, v[188:189] offset:24576
	v_pk_mul_f32 v[70:71], v[70:71], v[170:171] op_sel_hi:[1,0]
	v_pk_mul_f32 v[72:73], v[72:73], v[170:171] op_sel_hi:[1,0]
	v_cvt_pk_f16_f32 v190, v70, v71
	v_cvt_pk_f16_f32 v191, v72, v73
	ds_write_b64 v185, v[190:191] offset:24576
	v_pk_mul_f32 v[94:95], v[94:95], v[170:171] op_sel_hi:[1,0]
	v_pk_mul_f32 v[96:97], v[96:97], v[170:171] op_sel_hi:[1,0]
	v_cvt_pk_f16_f32 v192, v94, v95
	v_cvt_pk_f16_f32 v193, v96, v97
	ds_write_b64 v184, v[192:193] offset:24832
	v_pk_mul_f32 v[102:103], v[102:103], v[170:171] op_sel_hi:[1,0]
	v_pk_mul_f32 v[104:105], v[104:105], v[170:171] op_sel_hi:[1,0]
	v_cvt_pk_f16_f32 v194, v102, v103
	v_cvt_pk_f16_f32 v195, v104, v105
	ds_write_b64 v185, v[194:195] offset:24832
	v_pk_mul_f32 v[26:27], v[26:27], v[172:173] op_sel_hi:[1,0]
	v_pk_mul_f32 v[28:29], v[28:29], v[172:173] op_sel_hi:[1,0]
	v_cvt_pk_f16_f32 v188, v26, v27
	v_cvt_pk_f16_f32 v189, v28, v29
	ds_write_b64 v186, v[188:189]
	v_pk_mul_f32 v[30:31], v[30:31], v[172:173] op_sel_hi:[1,0]
	v_pk_mul_f32 v[32:33], v[32:33], v[172:173] op_sel_hi:[1,0]
	v_cvt_pk_f16_f32 v190, v30, v31
	v_cvt_pk_f16_f32 v191, v32, v33
	ds_write_b64 v187, v[190:191]
	v_pk_mul_f32 v[58:59], v[58:59], v[172:173] op_sel_hi:[1,0]
	v_pk_mul_f32 v[60:61], v[60:61], v[172:173] op_sel_hi:[1,0]
	v_cvt_pk_f16_f32 v192, v58, v59
	v_cvt_pk_f16_f32 v193, v60, v61
	ds_write_b64 v186, v[192:193] offset:256
	v_pk_mul_f32 v[62:63], v[62:63], v[172:173] op_sel_hi:[1,0]
	v_pk_mul_f32 v[64:65], v[64:65], v[172:173] op_sel_hi:[1,0]
	v_cvt_pk_f16_f32 v194, v62, v63
	v_cvt_pk_f16_f32 v195, v64, v65
	ds_write_b64 v187, v[194:195] offset:256
	v_pk_mul_f32 v[18:19], v[18:19], v[174:175] op_sel_hi:[1,0]
	v_pk_mul_f32 v[20:21], v[20:21], v[174:175] op_sel_hi:[1,0]
	v_cvt_pk_f16_f32 v188, v18, v19
	v_cvt_pk_f16_f32 v189, v20, v21
	ds_write_b64 v186, v[188:189] offset:8192
	v_pk_mul_f32 v[22:23], v[22:23], v[174:175] op_sel_hi:[1,0]
	v_pk_mul_f32 v[24:25], v[24:25], v[174:175] op_sel_hi:[1,0]
	v_cvt_pk_f16_f32 v190, v22, v23
	v_cvt_pk_f16_f32 v191, v24, v25
	ds_write_b64 v187, v[190:191] offset:8192
	v_pk_mul_f32 v[50:51], v[50:51], v[174:175] op_sel_hi:[1,0]
	v_pk_mul_f32 v[52:53], v[52:53], v[174:175] op_sel_hi:[1,0]
	v_cvt_pk_f16_f32 v192, v50, v51
	v_cvt_pk_f16_f32 v193, v52, v53
	ds_write_b64 v186, v[192:193] offset:8448
	v_pk_mul_f32 v[54:55], v[54:55], v[174:175] op_sel_hi:[1,0]
	v_pk_mul_f32 v[56:57], v[56:57], v[174:175] op_sel_hi:[1,0]
	v_cvt_pk_f16_f32 v194, v54, v55
	v_cvt_pk_f16_f32 v195, v56, v57
	ds_write_b64 v187, v[194:195] offset:8448
	v_pk_mul_f32 v[10:11], v[10:11], v[176:177] op_sel_hi:[1,0]
	v_pk_mul_f32 v[12:13], v[12:13], v[176:177] op_sel_hi:[1,0]
	v_cvt_pk_f16_f32 v188, v10, v11
	v_cvt_pk_f16_f32 v189, v12, v13
	ds_write_b64 v186, v[188:189] offset:16384
	v_pk_mul_f32 v[14:15], v[14:15], v[176:177] op_sel_hi:[1,0]
	v_pk_mul_f32 v[16:17], v[16:17], v[176:177] op_sel_hi:[1,0]
	v_cvt_pk_f16_f32 v190, v14, v15
	v_cvt_pk_f16_f32 v191, v16, v17
	ds_write_b64 v187, v[190:191] offset:16384
	v_pk_mul_f32 v[42:43], v[42:43], v[176:177] op_sel_hi:[1,0]
	v_pk_mul_f32 v[44:45], v[44:45], v[176:177] op_sel_hi:[1,0]
	v_cvt_pk_f16_f32 v192, v42, v43
	v_cvt_pk_f16_f32 v193, v44, v45
	ds_write_b64 v186, v[192:193] offset:16640
	v_pk_mul_f32 v[46:47], v[46:47], v[176:177] op_sel_hi:[1,0]
	v_pk_mul_f32 v[48:49], v[48:49], v[176:177] op_sel_hi:[1,0]
	v_cvt_pk_f16_f32 v194, v46, v47
	v_cvt_pk_f16_f32 v195, v48, v49
	ds_write_b64 v187, v[194:195] offset:16640
	v_pk_mul_f32 v[2:3], v[2:3], v[178:179] op_sel_hi:[1,0]
	v_pk_mul_f32 v[4:5], v[4:5], v[178:179] op_sel_hi:[1,0]
	v_cvt_pk_f16_f32 v188, v2, v3
	v_cvt_pk_f16_f32 v189, v4, v5
	ds_write_b64 v186, v[188:189] offset:24576
	v_pk_mul_f32 v[6:7], v[6:7], v[178:179] op_sel_hi:[1,0]
	v_pk_mul_f32 v[8:9], v[8:9], v[178:179] op_sel_hi:[1,0]
	v_cvt_pk_f16_f32 v190, v6, v7
	v_cvt_pk_f16_f32 v191, v8, v9
	ds_write_b64 v187, v[190:191] offset:24576
	v_pk_mul_f32 v[34:35], v[34:35], v[178:179] op_sel_hi:[1,0]
	v_pk_mul_f32 v[36:37], v[36:37], v[178:179] op_sel_hi:[1,0]
	v_cvt_pk_f16_f32 v192, v34, v35
	v_cvt_pk_f16_f32 v193, v36, v37
	ds_write_b64 v186, v[192:193] offset:24832
	v_pk_mul_f32 v[38:39], v[38:39], v[178:179] op_sel_hi:[1,0]
	v_pk_mul_f32 v[40:41], v[40:41], v[178:179] op_sel_hi:[1,0]
	v_cvt_pk_f16_f32 v194, v38, v39
	v_cvt_pk_f16_f32 v195, v40, v41
	ds_write_b64 v187, v[194:195] offset:24832
	s_waitcnt lgkmcnt(0)
	s_barrier
	ds_read_b128 v[2:5], v200
	ds_read_b128 v[6:9], v201 offset:1024
	ds_read_b128 v[10:13], v202 offset:2048
	ds_read_b128 v[14:17], v203 offset:3072
	ds_read_b128 v[18:21], v204 offset:4096
	ds_read_b128 v[22:25], v205 offset:5120
	ds_read_b128 v[26:29], v206 offset:6144
	ds_read_b128 v[30:33], v207 offset:7168
	ds_read_b128 v[34:37], v200 offset:8192
	ds_read_b128 v[38:41], v201 offset:9216
	ds_read_b128 v[42:45], v202 offset:10240
	ds_read_b128 v[46:49], v203 offset:11264
	ds_read_b128 v[50:53], v204 offset:12288
	ds_read_b128 v[54:57], v205 offset:13312
	ds_read_b128 v[58:61], v206 offset:14336
	ds_read_b128 v[62:65], v207 offset:15360
	s_waitcnt lgkmcnt(15)
	v_mov_b32_e32 v209, v208
	buffer_store_dwordx4 v[2:5], v209, s[68:71], 0 offen sc1
	s_waitcnt lgkmcnt(14)
	v_add_u32_e32 v210, 0x2000, v208
	buffer_store_dwordx4 v[6:9], v210, s[68:71], 0 offen sc1
	s_waitcnt lgkmcnt(13)
	v_add_u32_e32 v211, 0x4000, v208
	buffer_store_dwordx4 v[10:13], v211, s[68:71], 0 offen sc1
	s_waitcnt lgkmcnt(12)
	v_add_u32_e32 v212, 0x6000, v208
	buffer_store_dwordx4 v[14:17], v212, s[68:71], 0 offen sc1
	s_waitcnt lgkmcnt(11)
	v_add_u32_e32 v209, 0x8000, v208
	buffer_store_dwordx4 v[18:21], v209, s[68:71], 0 offen sc1
	s_waitcnt lgkmcnt(10)
	v_add_u32_e32 v210, 0xa000, v208
	buffer_store_dwordx4 v[22:25], v210, s[68:71], 0 offen sc1
	s_waitcnt lgkmcnt(9)
	v_add_u32_e32 v211, 0xc000, v208
	buffer_store_dwordx4 v[26:29], v211, s[68:71], 0 offen sc1
	s_waitcnt lgkmcnt(8)
	v_add_u32_e32 v212, 0xe000, v208
	buffer_store_dwordx4 v[30:33], v212, s[68:71], 0 offen sc1
	s_waitcnt lgkmcnt(7)
	v_add_u32_e32 v209, 0x10000, v208
	buffer_store_dwordx4 v[34:37], v209, s[68:71], 0 offen sc1
	s_waitcnt lgkmcnt(6)
	v_add_u32_e32 v210, 0x12000, v208
	buffer_store_dwordx4 v[38:41], v210, s[68:71], 0 offen sc1
	s_waitcnt lgkmcnt(5)
	v_add_u32_e32 v211, 0x14000, v208
	buffer_store_dwordx4 v[42:45], v211, s[68:71], 0 offen sc1
	s_waitcnt lgkmcnt(4)
	v_add_u32_e32 v212, 0x16000, v208
	buffer_store_dwordx4 v[46:49], v212, s[68:71], 0 offen sc1
	s_waitcnt lgkmcnt(3)
	v_add_u32_e32 v209, 0x18000, v208
	buffer_store_dwordx4 v[50:53], v209, s[68:71], 0 offen sc1
	s_waitcnt lgkmcnt(2)
	v_add_u32_e32 v210, 0x1a000, v208
	buffer_store_dwordx4 v[54:57], v210, s[68:71], 0 offen sc1
	s_waitcnt lgkmcnt(1)
	v_add_u32_e32 v211, 0x1c000, v208
	buffer_store_dwordx4 v[58:61], v211, s[68:71], 0 offen sc1
	s_waitcnt lgkmcnt(0)
	v_add_u32_e32 v212, 0x1e000, v208
	buffer_store_dwordx4 v[62:65], v212, s[68:71], 0 offen sc1
	s_waitcnt vmcnt(0)
	s_barrier
	s_and_saveexec_b64 s[4:5], s[2:3]
	s_xor_b64 s[2:3], exec, s[4:5]
	s_cbranch_execz .LBB2_367
	s_mov_b64 s[4:5], exec
	v_mbcnt_lo_u32_b32 v2, s4, 0
	v_mbcnt_hi_u32_b32 v2, s5, v2
	v_cmp_eq_u32_e32 vcc, 0, v2
	s_and_saveexec_b64 s[10:11], vcc
	s_xor_b64 s[10:11], exec, s[10:11]
	s_cbranch_execz .LBB2_366
	s_ashr_i32 s97, s96, 31
	s_lshl_b64 s[34:35], s[96:97], 2
	s_add_u32 s34, s22, s34
	s_addc_u32 s35, s23, s35
	s_bcnt1_i32_b64 s4, s[4:5]
	v_mov_b32_e32 v2, s4
	global_atomic_add v163, v2, s[34:35]

.LBB2_379:
	s_or_b64 exec, exec, s[4:5]
	s_lshl_b64 s[4:5], s[0:1], 23
	v_lshlrev_b32_e32 v5, 6, v5
	s_add_u32 s4, s26, s4
	v_sub_u32_e32 v4, v4, v5
	s_addc_u32 s5, s27, s5
	s_lshl_b32 s33, s33, 10
	s_lshl_b32 s10, s54, 20
	v_lshlrev_b32_e32 v3, 5, v3
	v_ashrrev_i16_sdwa v4, v183, sext(v4) dst_sel:DWORD dst_unused:UNUSED_PAD src0_sel:DWORD src1_sel:BYTE_0
	s_add_u32 s4, s4, s10
	v_and_b32_e32 v3, 32, v3
	v_bfe_i32 v4, v4, 0, 16
	s_addc_u32 s5, s5, 0
	s_add_i32 s52, s33, 0
	v_add_lshl_u32 v3, v3, v4, 1
	s_mov_b64 s[10:11], s[4:5]
	s_add_i32 s53, s52, 0x10000
	v_lshl_add_u32 v162, v2, 12, v3
	s_mov_b32 m0, s53
	s_barrier
	global_load_lds_dwordx4 v162, s[10:11]
	s_add_u32 s10, s10, 0x40000
	s_addc_u32 s11, s11, 0
	s_add_i32 s55, s52, 0x12000
	s_mov_b32 m0, s55
	s_add_i32 s86, s52, 0x2000
	global_load_lds_dwordx4 v162, s[10:11]
	s_add_u32 s10, s4, 0x80000
	s_waitcnt vmcnt(2)
	v_lshl_add_u32 v134, v6, 12, v3
	s_mov_b64 s[34:35], s[24:25]
	s_mov_b32 m0, s52
	s_addc_u32 s11, s5, 0
	v_lshl_add_u32 v136, v7, 12, v3
	s_mov_b64 s[56:57], s[10:11]
	global_load_lds_dwordx4 v134, s[34:35]
	s_mov_b32 m0, s86
	s_add_i32 s87, s52, 0x14000
	global_load_lds_dwordx4 v136, s[34:35]
	s_mov_b32 m0, s87
	v_lshl_add_u32 v132, v8, 12, v3
	global_load_lds_dwordx4 v162, s[56:57]
	s_add_u32 s56, s56, 0x40000
	s_addc_u32 s57, s57, 0
	s_add_i32 s88, s52, 0x16000
	s_mov_b32 m0, s88
	s_add_i32 s89, s52, 0x4000
	s_add_i32 s90, s52, 0x6000
	global_load_lds_dwordx4 v162, s[56:57]
	s_mov_b32 m0, s89
	v_lshl_add_u32 v130, v9, 12, v3
	global_load_lds_dwordx4 v132, s[34:35]
	s_mov_b32 m0, s90
	v_ashrrev_i32_e32 v2, 8, v141
	global_load_lds_dwordx4 v130, s[34:35]
	v_cmp_eq_u32_e32 vcc, 1, v2
	s_and_saveexec_b64 s[34:35], vcc
	s_cbranch_execz .LBB2_381
	s_barrier

.Lg2p_loop:
	ds_read_b128 v[140:143], v138
	ds_read_b128 v[154:157], v138 offset:1024
	ds_read_b128 v[158:161], v138 offset:2048
	ds_read_b128 v[164:167], v138 offset:3072
	s_lshl_b32 vcc_hi, s57, 7
	s_add_u32 s58, s88, vcc_hi
	s_addc_u32 s59, s89, 0
	s_add_u32 s82, s58, 0x80
	s_addc_u32 s83, s59, 0
	s_add_i32 s59, s97, 0xc000
	v_lshl_add_u64 v[144:145], s[82:83], 0, v[162:163]
	s_add_u32 s82, s82, 0x20000
	s_mov_b32 m0, s59
	s_addc_u32 s83, s83, 0
	s_add_i32 s58, s97, 0xe000
	ds_read_b128 v[168:171], v134
	ds_read_b128 v[172:175], v134 offset:1024
	ds_read_b128 v[176:179], v133
	ds_read_b128 v[184:187], v133 offset:1024
	ds_read_b128 v[188:191], v131
	ds_read_b128 v[192:195], v131 offset:1024
	ds_read_b128 v[196:199], v130
	ds_read_b128 v[200:203], v130 offset:1024
	global_load_lds_dwordx4 v[144:145], off
	s_mov_b32 m0, s58
	v_lshl_add_u64 v[144:145], s[82:83], 0, v[162:163]
	global_load_lds_dwordx4 v[144:145], off
	s_waitcnt lgkmcnt(8)
	s_barrier
	s_setprio 1
	s_waitcnt lgkmcnt(0)
	s_bitcmp1_b32 s100, 0
	s_cbranch_scc1 .Lg2p_skip1
	v_mfma_f32_16x16x32_f16 v[102:105], v[140:143], v[168:171], v[102:105]
	v_mfma_f32_16x16x32_f16 v[98:101], v[158:161], v[168:171], v[98:101]
	v_mfma_f32_16x16x32_f16 v[126:129], v[140:143], v[176:179], v[126:129]
	v_mfma_f32_16x16x32_f16 v[122:125], v[158:161], v[176:179], v[122:125]
	v_mfma_f32_16x16x32_f16 v[118:121], v[140:143], v[188:191], v[118:121]
	v_mfma_f32_16x16x32_f16 v[114:117], v[158:161], v[188:191], v[114:117]
	v_mfma_f32_16x16x32_f16 v[110:113], v[140:143], v[196:199], v[110:113]
	v_mfma_f32_16x16x32_f16 v[106:109], v[158:161], v[196:199], v[106:109]
	v_mfma_f32_16x16x32_f16 v[102:105], v[154:157], v[172:175], v[102:105]
	v_mfma_f32_16x16x32_f16 v[98:101], v[164:167], v[172:175], v[98:101]
	v_mfma_f32_16x16x32_f16 v[126:129], v[154:157], v[184:187], v[126:129]
	v_mfma_f32_16x16x32_f16 v[122:125], v[164:167], v[184:187], v[122:125]
	v_mfma_f32_16x16x32_f16 v[118:121], v[154:157], v[192:195], v[118:121]
	v_mfma_f32_16x16x32_f16 v[114:117], v[164:167], v[192:195], v[114:117]
	v_mfma_f32_16x16x32_f16 v[110:113], v[154:157], v[200:203], v[110:113]
	v_mfma_f32_16x16x32_f16 v[106:109], v[164:167], v[200:203], v[106:109]
.Lg2p_skip1:
	s_setprio 0
	s_barrier
	s_add_i32 vcc_lo, s57, 2
	s_lshl_b32 s78, vcc_lo, 7
	s_add_u32 s82, s92, s78
	s_addc_u32 s83, s93, 0
	s_mov_b32 m0, s84
	v_lshl_add_u64 v[144:145], s[82:83], 0, v[162:163]
	s_add_u32 s82, s82, 0x20000
	s_addc_u32 s83, s83, 0
	ds_read_b128 v[204:207], v137
	ds_read_b128 v[208:211], v137 offset:1024
	ds_read_b128 v[212:215], v137 offset:2048
	ds_read_b128 v[216:219], v137 offset:3072
	global_load_lds_dwordx4 v[144:145], off
	s_mov_b32 m0, s94
	v_lshl_add_u64 v[144:145], s[82:83], 0, v[162:163]
	global_load_lds_dwordx4 v[144:145], off
	s_barrier
	s_setprio 1
	s_waitcnt lgkmcnt(0)
	s_bitcmp1_b32 s100, 0
	s_cbranch_scc1 .Lg2p_skip2
	v_mfma_f32_16x16x32_f16 v[94:97], v[204:207], v[168:171], v[94:97]
	v_mfma_f32_16x16x32_f16 v[90:93], v[212:215], v[168:171], v[90:93]
	v_mfma_f32_16x16x32_f16 v[86:89], v[204:207], v[176:179], v[86:89]
	v_mfma_f32_16x16x32_f16 v[82:85], v[212:215], v[176:179], v[82:85]
	v_mfma_f32_16x16x32_f16 v[78:81], v[204:207], v[188:191], v[78:81]
	v_mfma_f32_16x16x32_f16 v[74:77], v[212:215], v[188:191], v[74:77]
	v_mfma_f32_16x16x32_f16 v[70:73], v[204:207], v[196:199], v[70:73]
	v_mfma_f32_16x16x32_f16 v[66:69], v[212:215], v[196:199], v[66:69]
	v_mfma_f32_16x16x32_f16 v[94:97], v[208:211], v[172:175], v[94:97]
	v_mfma_f32_16x16x32_f16 v[90:93], v[216:219], v[172:175], v[90:93]
	v_mfma_f32_16x16x32_f16 v[86:89], v[208:211], v[184:187], v[86:89]
	v_mfma_f32_16x16x32_f16 v[82:85], v[216:219], v[184:187], v[82:85]
	v_mfma_f32_16x16x32_f16 v[78:81], v[208:211], v[192:195], v[78:81]
	v_mfma_f32_16x16x32_f16 v[74:77], v[216:219], v[192:195], v[74:77]
	v_mfma_f32_16x16x32_f16 v[70:73], v[208:211], v[200:203], v[70:73]
	v_mfma_f32_16x16x32_f16 v[66:69], v[216:219], v[200:203], v[66:69]
.Lg2p_skip2:
	s_setprio 0
	s_add_u32 s82, s90, s78
	s_addc_u32 s83, s91, 0
	s_mov_b32 m0, s97
	v_lshl_add_u64 v[144:145], s[82:83], 0, v[162:163]
	s_add_u32 s82, s82, 0x20000
	s_addc_u32 s83, s83, 0
	s_barrier
	ds_read_b128 v[168:171], v134 offset:16384
	ds_read_b128 v[172:175], v134 offset:17408
	ds_read_b128 v[176:179], v133 offset:16384
	ds_read_b128 v[184:187], v133 offset:17408
	ds_read_b128 v[188:191], v131 offset:16384
	ds_read_b128 v[192:195], v131 offset:17408
	ds_read_b128 v[196:199], v130 offset:16384
	ds_read_b128 v[200:203], v130 offset:17408
	global_load_lds_dwordx4 v[144:145], off
	s_mov_b32 m0, s99
	v_lshl_add_u64 v[144:145], s[82:83], 0, v[162:163]
	global_load_lds_dwordx4 v[144:145], off
	s_barrier
	s_setprio 1
	s_waitcnt lgkmcnt(0)
	s_bitcmp1_b32 s100, 1
	s_cbranch_scc1 .Lg2p_skip3
	v_mfma_f32_16x16x32_f16 v[62:65], v[140:143], v[168:171], v[62:65]
	v_mfma_f32_16x16x32_f16 v[58:61], v[158:161], v[168:171], v[58:61]
	v_mfma_f32_16x16x32_f16 v[54:57], v[140:143], v[176:179], v[54:57]
	v_mfma_f32_16x16x32_f16 v[50:53], v[158:161], v[176:179], v[50:53]
	v_mfma_f32_16x16x32_f16 v[46:49], v[140:143], v[188:191], v[46:49]
	v_mfma_f32_16x16x32_f16 v[42:45], v[158:161], v[188:191], v[42:45]
	v_mfma_f32_16x16x32_f16 v[38:41], v[140:143], v[196:199], v[38:41]
	v_mfma_f32_16x16x32_f16 v[30:33], v[158:161], v[196:199], v[30:33]
	v_mfma_f32_16x16x32_f16 v[62:65], v[154:157], v[172:175], v[62:65]
	v_mfma_f32_16x16x32_f16 v[58:61], v[164:167], v[172:175], v[58:61]
	v_mfma_f32_16x16x32_f16 v[54:57], v[154:157], v[184:187], v[54:57]
	v_mfma_f32_16x16x32_f16 v[50:53], v[164:167], v[184:187], v[50:53]
	v_mfma_f32_16x16x32_f16 v[46:49], v[154:157], v[192:195], v[46:49]
	v_mfma_f32_16x16x32_f16 v[42:45], v[164:167], v[192:195], v[42:45]
	v_mfma_f32_16x16x32_f16 v[38:41], v[154:157], v[200:203], v[38:41]
	v_mfma_f32_16x16x32_f16 v[30:33], v[164:167], v[200:203], v[30:33]
.Lg2p_skip3:
	s_setprio 0
	s_barrier
	s_add_u32 s82, s34, s78
	s_addc_u32 s83, s35, 0
	s_mov_b32 m0, s95
	v_lshl_add_u64 v[140:141], s[82:83], 0, v[162:163]
	s_add_u32 s82, s82, 0x20000
	s_addc_u32 s83, s83, 0
	global_load_lds_dwordx4 v[140:141], off
	s_mov_b32 m0, s33
	v_lshl_add_u64 v[140:141], s[82:83], 0, v[162:163]
	global_load_lds_dwordx4 v[140:141], off
	s_waitcnt vmcnt(6)
	s_barrier
	s_setprio 1
	s_bitcmp1_b32 s100, 1
	s_cbranch_scc1 .Lg2p_skip4
	v_mfma_f32_16x16x32_f16 v[34:37], v[204:207], v[168:171], v[34:37]
	v_mfma_f32_16x16x32_f16 v[26:29], v[212:215], v[168:171], v[26:29]
	v_mfma_f32_16x16x32_f16 v[22:25], v[204:207], v[176:179], v[22:25]
	v_mfma_f32_16x16x32_f16 v[18:21], v[212:215], v[176:179], v[18:21]
	v_mfma_f32_16x16x32_f16 v[14:17], v[204:207], v[188:191], v[14:17]
	v_mfma_f32_16x16x32_f16 v[10:13], v[212:215], v[188:191], v[10:13]
	v_mfma_f32_16x16x32_f16 v[6:9], v[204:207], v[196:199], v[6:9]
	v_mfma_f32_16x16x32_f16 v[2:5], v[212:215], v[196:199], v[2:5]
	v_mfma_f32_16x16x32_f16 v[34:37], v[208:211], v[172:175], v[34:37]
	v_mfma_f32_16x16x32_f16 v[26:29], v[216:219], v[172:175], v[26:29]
	v_mfma_f32_16x16x32_f16 v[22:25], v[208:211], v[184:187], v[22:25]
	v_mfma_f32_16x16x32_f16 v[18:21], v[216:219], v[184:187], v[18:21]
	v_mfma_f32_16x16x32_f16 v[14:17], v[208:211], v[192:195], v[14:17]
	v_mfma_f32_16x16x32_f16 v[10:13], v[216:219], v[192:195], v[10:13]
	v_mfma_f32_16x16x32_f16 v[6:9], v[208:211], v[200:203], v[6:9]
	v_mfma_f32_16x16x32_f16 v[2:5], v[216:219], v[200:203], v[2:5]
.Lg2p_skip4:
	s_setprio 0
	s_barrier
	ds_read_b128 v[140:143], v136
	ds_read_b128 v[154:157], v136 offset:1024
	ds_read_b128 v[158:161], v136 offset:2048
	ds_read_b128 v[164:167], v136 offset:3072
	s_add_u32 s82, s88, s78
	s_addc_u32 s83, s89, 0
	s_mov_b32 m0, s11
	v_lshl_add_u64 v[144:145], s[82:83], 0, v[162:163]
	s_add_u32 s82, s82, 0x20000
	s_addc_u32 s83, s83, 0
	ds_read_b128 v[168:171], v134 offset:32768
	ds_read_b128 v[172:175], v134 offset:33792
	ds_read_b128 v[176:179], v133 offset:32768
	ds_read_b128 v[184:187], v133 offset:33792
	ds_read_b128 v[188:191], v131 offset:32768
	ds_read_b128 v[192:195], v131 offset:33792
	ds_read_b128 v[196:199], v130 offset:32768
	ds_read_b128 v[200:203], v130 offset:33792
	global_load_lds_dwordx4 v[144:145], off
	s_mov_b32 m0, s56
	v_lshl_add_u64 v[144:145], s[82:83], 0, v[162:163]
	global_load_lds_dwordx4 v[144:145], off
	s_waitcnt lgkmcnt(8)
	s_barrier
	s_setprio 1
	s_waitcnt lgkmcnt(0)
	s_bitcmp1_b32 s100, 0
	s_cbranch_scc1 .Lg2p_skip5
	v_mfma_f32_16x16x32_f16 v[102:105], v[140:143], v[168:171], v[102:105]
	v_mfma_f32_16x16x32_f16 v[98:101], v[158:161], v[168:171], v[98:101]
	v_mfma_f32_16x16x32_f16 v[126:129], v[140:143], v[176:179], v[126:129]
	v_mfma_f32_16x16x32_f16 v[122:125], v[158:161], v[176:179], v[122:125]
	v_mfma_f32_16x16x32_f16 v[118:121], v[140:143], v[188:191], v[118:121]
	v_mfma_f32_16x16x32_f16 v[114:117], v[158:161], v[188:191], v[114:117]
	v_mfma_f32_16x16x32_f16 v[110:113], v[140:143], v[196:199], v[110:113]
	v_mfma_f32_16x16x32_f16 v[106:109], v[158:161], v[196:199], v[106:109]
	v_mfma_f32_16x16x32_f16 v[102:105], v[154:157], v[172:175], v[102:105]
	v_mfma_f32_16x16x32_f16 v[98:101], v[164:167], v[172:175], v[98:101]
	v_mfma_f32_16x16x32_f16 v[126:129], v[154:157], v[184:187], v[126:129]
	v_mfma_f32_16x16x32_f16 v[122:125], v[164:167], v[184:187], v[122:125]
	v_mfma_f32_16x16x32_f16 v[118:121], v[154:157], v[192:195], v[118:121]
	v_mfma_f32_16x16x32_f16 v[114:117], v[164:167], v[192:195], v[114:117]
	v_mfma_f32_16x16x32_f16 v[110:113], v[154:157], v[200:203], v[110:113]
	v_mfma_f32_16x16x32_f16 v[106:109], v[164:167], v[200:203], v[106:109]
.Lg2p_skip5:
	s_setprio 0
	s_barrier
	s_add_u32 s78, s92, vcc_hi
	s_addc_u32 s79, s93, 0
	s_add_u32 s82, s78, 0x180
	s_addc_u32 s83, s79, 0
	s_add_i32 m0, s97, 0x18000
	v_lshl_add_u64 v[144:145], s[82:83], 0, v[162:163]
	s_add_u32 s82, s82, 0x20000
	s_addc_u32 s83, s83, 0
	ds_read_b128 v[204:207], v135
	ds_read_b128 v[208:211], v135 offset:1024
	ds_read_b128 v[212:215], v135 offset:2048
	ds_read_b128 v[216:219], v135 offset:3072
	global_load_lds_dwordx4 v[144:145], off
	s_add_i32 m0, s97, 0x1a000
	v_lshl_add_u64 v[144:145], s[82:83], 0, v[162:163]
	global_load_lds_dwordx4 v[144:145], off
	s_barrier
	s_setprio 1
	s_waitcnt lgkmcnt(0)
	s_bitcmp1_b32 s100, 0
	s_cbranch_scc1 .Lg2p_skip6
	v_mfma_f32_16x16x32_f16 v[94:97], v[204:207], v[168:171], v[94:97]
	v_mfma_f32_16x16x32_f16 v[90:93], v[212:215], v[168:171], v[90:93]
	v_mfma_f32_16x16x32_f16 v[86:89], v[204:207], v[176:179], v[86:89]
	v_mfma_f32_16x16x32_f16 v[82:85], v[212:215], v[176:179], v[82:85]
	v_mfma_f32_16x16x32_f16 v[78:81], v[204:207], v[188:191], v[78:81]
	v_mfma_f32_16x16x32_f16 v[74:77], v[212:215], v[188:191], v[74:77]
	v_mfma_f32_16x16x32_f16 v[70:73], v[204:207], v[196:199], v[70:73]
	v_mfma_f32_16x16x32_f16 v[66:69], v[212:215], v[196:199], v[66:69]
	v_mfma_f32_16x16x32_f16 v[94:97], v[208:211], v[172:175], v[94:97]
	v_mfma_f32_16x16x32_f16 v[90:93], v[216:219], v[172:175], v[90:93]
	v_mfma_f32_16x16x32_f16 v[86:89], v[208:211], v[184:187], v[86:89]
	v_mfma_f32_16x16x32_f16 v[82:85], v[216:219], v[184:187], v[82:85]
	v_mfma_f32_16x16x32_f16 v[78:81], v[208:211], v[192:195], v[78:81]
	v_mfma_f32_16x16x32_f16 v[74:77], v[216:219], v[192:195], v[74:77]
	v_mfma_f32_16x16x32_f16 v[70:73], v[208:211], v[200:203], v[70:73]
	v_mfma_f32_16x16x32_f16 v[66:69], v[216:219], v[200:203], v[66:69]
.Lg2p_skip6:
	s_setprio 0
	s_add_u32 s78, s90, vcc_hi
	s_addc_u32 s79, s91, 0
	s_add_u32 s82, s78, 0x180
	s_addc_u32 s83, s79, 0
	s_mov_b32 m0, s52
	v_lshl_add_u64 v[144:145], s[82:83], 0, v[162:163]
	s_add_u32 s82, s82, 0x20000
	s_addc_u32 s83, s83, 0
	s_barrier
	ds_read_b128 v[168:171], v134 offset:49152
	ds_read_b128 v[172:175], v134 offset:50176
	ds_read_b128 v[176:179], v133 offset:49152
	ds_read_b128 v[184:187], v133 offset:50176
	ds_read_b128 v[188:191], v131 offset:49152
	ds_read_b128 v[192:195], v131 offset:50176
	ds_read_b128 v[196:199], v130 offset:49152
	ds_read_b128 v[200:203], v130 offset:50176
	global_load_lds_dwordx4 v[144:145], off
	s_mov_b32 m0, s53
	v_lshl_add_u64 v[144:145], s[82:83], 0, v[162:163]
	global_load_lds_dwordx4 v[144:145], off
	s_barrier
	s_setprio 1
	s_waitcnt lgkmcnt(0)
	s_bitcmp1_b32 s100, 1
	s_cbranch_scc1 .Lg2p_skip7
	v_mfma_f32_16x16x32_f16 v[62:65], v[140:143], v[168:171], v[62:65]
	v_mfma_f32_16x16x32_f16 v[58:61], v[158:161], v[168:171], v[58:61]
	v_mfma_f32_16x16x32_f16 v[54:57], v[140:143], v[176:179], v[54:57]
	v_mfma_f32_16x16x32_f16 v[50:53], v[158:161], v[176:179], v[50:53]
	v_mfma_f32_16x16x32_f16 v[46:49], v[140:143], v[188:191], v[46:49]
	v_mfma_f32_16x16x32_f16 v[42:45], v[158:161], v[188:191], v[42:45]
	v_mfma_f32_16x16x32_f16 v[38:41], v[140:143], v[196:199], v[38:41]
	v_mfma_f32_16x16x32_f16 v[30:33], v[158:161], v[196:199], v[30:33]
	v_mfma_f32_16x16x32_f16 v[62:65], v[154:157], v[172:175], v[62:65]
	v_mfma_f32_16x16x32_f16 v[58:61], v[164:167], v[172:175], v[58:61]
	v_mfma_f32_16x16x32_f16 v[54:57], v[154:157], v[184:187], v[54:57]
	v_mfma_f32_16x16x32_f16 v[50:53], v[164:167], v[184:187], v[50:53]
	v_mfma_f32_16x16x32_f16 v[46:49], v[154:157], v[192:195], v[46:49]
	v_mfma_f32_16x16x32_f16 v[42:45], v[164:167], v[192:195], v[42:45]
	v_mfma_f32_16x16x32_f16 v[38:41], v[154:157], v[200:203], v[38:41]
	v_mfma_f32_16x16x32_f16 v[30:33], v[164:167], v[200:203], v[30:33]
.Lg2p_skip7:
	s_setprio 0
	s_barrier
	s_add_u32 s78, s34, vcc_hi
	s_addc_u32 s79, s35, 0
	s_add_u32 s82, s78, 0x180
	s_addc_u32 s83, s79, 0
	s_add_i32 m0, s97, 0x1c000
	v_lshl_add_u64 v[140:141], s[82:83], 0, v[162:163]
	s_add_u32 s82, s82, 0x20000
	s_addc_u32 s83, s83, 0
	global_load_lds_dwordx4 v[140:141], off
	s_add_i32 m0, s97, 0x1e000
	v_lshl_add_u64 v[140:141], s[82:83], 0, v[162:163]
	global_load_lds_dwordx4 v[140:141], off
	s_waitcnt vmcnt(6)
	s_barrier
	s_setprio 1
	s_bitcmp1_b32 s100, 1
	s_cbranch_scc1 .Lg2p_skip8
	v_mfma_f32_16x16x32_f16 v[34:37], v[204:207], v[168:171], v[34:37]
	v_mfma_f32_16x16x32_f16 v[26:29], v[212:215], v[168:171], v[26:29]
	v_mfma_f32_16x16x32_f16 v[22:25], v[204:207], v[176:179], v[22:25]
	v_mfma_f32_16x16x32_f16 v[18:21], v[212:215], v[176:179], v[18:21]
	v_mfma_f32_16x16x32_f16 v[14:17], v[204:207], v[188:191], v[14:17]
	v_mfma_f32_16x16x32_f16 v[10:13], v[212:215], v[188:191], v[10:13]
	v_mfma_f32_16x16x32_f16 v[6:9], v[204:207], v[196:199], v[6:9]
	v_mfma_f32_16x16x32_f16 v[2:5], v[212:215], v[196:199], v[2:5]
	v_mfma_f32_16x16x32_f16 v[34:37], v[208:211], v[172:175], v[34:37]
	v_mfma_f32_16x16x32_f16 v[26:29], v[216:219], v[172:175], v[26:29]
	v_mfma_f32_16x16x32_f16 v[22:25], v[208:211], v[184:187], v[22:25]
	v_mfma_f32_16x16x32_f16 v[18:21], v[216:219], v[184:187], v[18:21]
	v_mfma_f32_16x16x32_f16 v[14:17], v[208:211], v[192:195], v[14:17]
	v_mfma_f32_16x16x32_f16 v[10:13], v[216:219], v[192:195], v[10:13]
	v_mfma_f32_16x16x32_f16 v[6:9], v[208:211], v[200:203], v[6:9]
	v_mfma_f32_16x16x32_f16 v[2:5], v[216:219], v[200:203], v[2:5]
.Lg2p_skip8:
	s_setprio 0
	s_cmp_lt_u32 s57, 12
	s_mov_b32 s57, vcc_lo
	s_barrier
	s_cbranch_scc1 .Lg2p_loop
	s_add_u32 s34, s88, 0x780
	s_addc_u32 s35, s89, 0
	ds_read_b128 v[140:143], v138
	ds_read_b128 v[154:157], v138 offset:1024
	ds_read_b128 v[158:161], v138 offset:2048
	ds_read_b128 v[164:167], v138 offset:3072
	ds_read_b128 v[168:171], v134
	ds_read_b128 v[172:175], v134 offset:1024
	ds_read_b128 v[176:179], v133
	ds_read_b128 v[184:187], v133 offset:1024
	ds_read_b128 v[188:191], v131
	ds_read_b128 v[192:195], v131 offset:1024
	ds_read_b128 v[196:199], v130
	ds_read_b128 v[200:203], v130 offset:1024
	v_lshl_add_u64 v[138:139], s[34:35], 0, v[162:163]
	s_add_u32 s34, s34, 0x20000
	s_mov_b32 m0, s59
	s_addc_u32 s35, s35, 0
	global_load_lds_dwordx4 v[138:139], off
	s_mov_b32 m0, s58
	v_lshl_add_u64 v[138:139], s[34:35], 0, v[162:163]
	global_load_lds_dwordx4 v[138:139], off
	s_barrier
	s_setprio 1
	s_waitcnt lgkmcnt(0)
	s_bitcmp1_b32 s100, 0
	s_cbranch_scc1 .Lg2p_skip9
	v_mfma_f32_16x16x32_f16 v[102:105], v[140:143], v[168:171], v[102:105]
	v_mfma_f32_16x16x32_f16 v[98:101], v[158:161], v[168:171], v[98:101]
	v_mfma_f32_16x16x32_f16 v[126:129], v[140:143], v[176:179], v[126:129]
	v_mfma_f32_16x16x32_f16 v[122:125], v[158:161], v[176:179], v[122:125]
	v_mfma_f32_16x16x32_f16 v[118:121], v[140:143], v[188:191], v[118:121]
	v_mfma_f32_16x16x32_f16 v[114:117], v[158:161], v[188:191], v[114:117]
	v_mfma_f32_16x16x32_f16 v[110:113], v[140:143], v[196:199], v[110:113]
	v_mfma_f32_16x16x32_f16 v[106:109], v[158:161], v[196:199], v[106:109]
	v_mfma_f32_16x16x32_f16 v[102:105], v[154:157], v[172:175], v[102:105]
	v_mfma_f32_16x16x32_f16 v[98:101], v[164:167], v[172:175], v[98:101]
	v_mfma_f32_16x16x32_f16 v[126:129], v[154:157], v[184:187], v[126:129]
	v_mfma_f32_16x16x32_f16 v[122:125], v[164:167], v[184:187], v[122:125]
	v_mfma_f32_16x16x32_f16 v[118:121], v[154:157], v[192:195], v[118:121]
	v_mfma_f32_16x16x32_f16 v[114:117], v[164:167], v[192:195], v[114:117]
	v_mfma_f32_16x16x32_f16 v[110:113], v[154:157], v[200:203], v[110:113]
	v_mfma_f32_16x16x32_f16 v[106:109], v[164:167], v[200:203], v[106:109]
.Lg2p_skip9:
	s_setprio 0
	s_barrier
	ds_read_b128 v[204:207], v137
	ds_read_b128 v[208:211], v137 offset:1024
	ds_read_b128 v[212:215], v137 offset:2048
	ds_read_b128 v[216:219], v137 offset:3072
	s_barrier
	s_setprio 1
	s_waitcnt lgkmcnt(0)
	s_bitcmp1_b32 s100, 0
	s_cbranch_scc1 .Lg2p_skip10
	v_mfma_f32_16x16x32_f16 v[94:97], v[204:207], v[168:171], v[94:97]
	v_mfma_f32_16x16x32_f16 v[94:97], v[208:211], v[172:175], v[94:97]
	v_mfma_f32_16x16x32_f16 v[90:93], v[212:215], v[168:171], v[90:93]
	v_mfma_f32_16x16x32_f16 v[86:89], v[204:207], v[176:179], v[86:89]
	v_mfma_f32_16x16x32_f16 v[82:85], v[212:215], v[176:179], v[82:85]
	v_mfma_f32_16x16x32_f16 v[78:81], v[204:207], v[188:191], v[78:81]
	v_mfma_f32_16x16x32_f16 v[74:77], v[212:215], v[188:191], v[74:77]
	v_mfma_f32_16x16x32_f16 v[70:73], v[204:207], v[196:199], v[70:73]
	v_mfma_f32_16x16x32_f16 v[66:69], v[212:215], v[196:199], v[66:69]
	v_mfma_f32_16x16x32_f16 v[168:171], v[216:219], v[172:175], v[90:93]
	v_mfma_f32_16x16x32_f16 v[172:175], v[208:211], v[184:187], v[86:89]
	v_mfma_f32_16x16x32_f16 v[176:179], v[216:219], v[184:187], v[82:85]
	v_mfma_f32_16x16x32_f16 v[184:187], v[208:211], v[192:195], v[78:81]
	v_mfma_f32_16x16x32_f16 v[188:191], v[216:219], v[192:195], v[74:77]
	v_mfma_f32_16x16x32_f16 v[192:195], v[208:211], v[200:203], v[70:73]
	v_mfma_f32_16x16x32_f16 v[196:199], v[216:219], v[200:203], v[66:69]
.Lg2p_skip10:
	s_setprio 0
	s_barrier
	s_nop 0
	ds_read_b128 v[66:69], v134 offset:16384
	ds_read_b128 v[70:73], v134 offset:17408
	ds_read_b128 v[74:77], v133 offset:16384
	ds_read_b128 v[78:81], v133 offset:17408
	ds_read_b128 v[82:85], v131 offset:16384
	ds_read_b128 v[86:89], v131 offset:17408
	ds_read_b128 v[90:93], v130 offset:16384
	ds_read_b128 v[200:203], v130 offset:17408
	s_waitcnt vmcnt(4)
	s_barrier
	s_setprio 1
	s_waitcnt lgkmcnt(0)
	s_bitcmp1_b32 s100, 1
	s_cbranch_scc1 .Lg2p_skip11
	v_mfma_f32_16x16x32_f16 v[62:65], v[140:143], v[66:69], v[62:65]
	v_mfma_f32_16x16x32_f16 v[58:61], v[158:161], v[66:69], v[58:61]
	v_mfma_f32_16x16x32_f16 v[54:57], v[140:143], v[74:77], v[54:57]
	v_mfma_f32_16x16x32_f16 v[50:53], v[158:161], v[74:77], v[50:53]
	v_mfma_f32_16x16x32_f16 v[46:49], v[140:143], v[82:85], v[46:49]
	v_mfma_f32_16x16x32_f16 v[42:45], v[158:161], v[82:85], v[42:45]
	v_mfma_f32_16x16x32_f16 v[38:41], v[140:143], v[90:93], v[38:41]
	v_mfma_f32_16x16x32_f16 v[62:65], v[154:157], v[70:73], v[62:65]
	v_mfma_f32_16x16x32_f16 v[58:61], v[164:167], v[70:73], v[58:61]
	v_mfma_f32_16x16x32_f16 v[54:57], v[154:157], v[78:81], v[54:57]
	v_mfma_f32_16x16x32_f16 v[50:53], v[164:167], v[78:81], v[50:53]
	v_mfma_f32_16x16x32_f16 v[46:49], v[154:157], v[86:89], v[46:49]
	v_mfma_f32_16x16x32_f16 v[42:45], v[164:167], v[86:89], v[42:45]
	v_mfma_f32_16x16x32_f16 v[38:41], v[154:157], v[200:203], v[38:41]
	v_mfma_f32_16x16x32_f16 v[30:33], v[158:161], v[90:93], v[30:33]
	v_mfma_f32_16x16x32_f16 v[138:141], v[164:167], v[200:203], v[30:33]
.Lg2p_skip11:
	s_setprio 0
	s_setprio 1
	s_bitcmp1_b32 s100, 1
	s_cbranch_scc1 .Lg2p_skip12
	v_mfma_f32_16x16x32_f16 v[30:33], v[204:207], v[66:69], v[34:37]
	v_mfma_f32_16x16x32_f16 v[34:37], v[208:211], v[70:73], v[30:33]
	v_mfma_f32_16x16x32_f16 v[26:29], v[212:215], v[66:69], v[26:29]
	v_mfma_f32_16x16x32_f16 v[22:25], v[204:207], v[74:77], v[22:25]
	v_mfma_f32_16x16x32_f16 v[18:21], v[212:215], v[74:77], v[18:21]
	v_mfma_f32_16x16x32_f16 v[14:17], v[204:207], v[82:85], v[14:17]
	v_mfma_f32_16x16x32_f16 v[10:13], v[212:215], v[82:85], v[10:13]
	v_mfma_f32_16x16x32_f16 v[6:9], v[204:207], v[90:93], v[6:9]
	v_mfma_f32_16x16x32_f16 v[2:5], v[212:215], v[90:93], v[2:5]
	v_mfma_f32_16x16x32_f16 v[142:145], v[216:219], v[70:73], v[26:29]
	v_mfma_f32_16x16x32_f16 v[154:157], v[208:211], v[78:81], v[22:25]
	v_mfma_f32_16x16x32_f16 v[158:161], v[216:219], v[78:81], v[18:21]
	v_mfma_f32_16x16x32_f16 v[164:167], v[208:211], v[86:89], v[14:17]
	v_mfma_f32_16x16x32_f16 v[220:223], v[216:219], v[86:89], v[10:13]
	v_mfma_f32_16x16x32_f16 v[204:207], v[208:211], v[200:203], v[6:9]
	v_mfma_f32_16x16x32_f16 v[200:203], v[216:219], v[200:203], v[2:5]
.Lg2p_skip12:
	s_setprio 0
	s_barrier
	s_nop 0
	ds_read_b128 v[2:5], v136
	ds_read_b128 v[6:9], v136 offset:1024
	ds_read_b128 v[208:211], v136 offset:2048
	ds_read_b128 v[212:215], v136 offset:3072
	ds_read_b128 v[10:13], v134 offset:32768
	ds_read_b128 v[14:17], v134 offset:33792
	ds_read_b128 v[18:21], v133 offset:32768
	ds_read_b128 v[22:25], v133 offset:33792
	ds_read_b128 v[26:29], v131 offset:32768
	ds_read_b128 v[30:33], v131 offset:33792
	ds_read_b128 v[216:219], v130 offset:32768
	ds_read_b128 v[224:227], v130 offset:33792
	s_waitcnt vmcnt(2)
	s_barrier
	s_setprio 1
	s_waitcnt lgkmcnt(0)
	s_bitcmp1_b32 s100, 0
	s_cbranch_scc1 .Lg2p_skip13
	v_mfma_f32_16x16x32_f16 v[66:69], v[2:5], v[10:13], v[102:105]
	v_mfma_f32_16x16x32_f16 v[90:93], v[6:9], v[14:17], v[66:69]
	v_mfma_f32_16x16x32_f16 v[66:69], v[208:211], v[10:13], v[98:101]
	v_mfma_f32_16x16x32_f16 v[98:101], v[212:215], v[14:17], v[66:69]
	v_mfma_f32_16x16x32_f16 v[66:69], v[2:5], v[18:21], v[126:129]
	v_mfma_f32_16x16x32_f16 v[82:85], v[6:9], v[22:25], v[66:69]
	v_mfma_f32_16x16x32_f16 v[66:69], v[208:211], v[18:21], v[122:125]
	v_mfma_f32_16x16x32_f16 v[86:89], v[212:215], v[22:25], v[66:69]
	v_mfma_f32_16x16x32_f16 v[66:69], v[2:5], v[26:29], v[118:121]
	v_mfma_f32_16x16x32_f16 v[74:77], v[6:9], v[30:33], v[66:69]
	v_mfma_f32_16x16x32_f16 v[66:69], v[208:211], v[26:29], v[114:117]
	v_mfma_f32_16x16x32_f16 v[78:81], v[212:215], v[30:33], v[66:69]
	v_mfma_f32_16x16x32_f16 v[66:69], v[2:5], v[216:219], v[110:113]
	v_mfma_f32_16x16x32_f16 v[70:73], v[208:211], v[216:219], v[106:109]
	v_mfma_f32_16x16x32_f16 v[66:69], v[6:9], v[224:227], v[66:69]
	v_mfma_f32_16x16x32_f16 v[70:73], v[212:215], v[224:227], v[70:73]
.Lg2p_skip13:
	s_setprio 0
	s_barrier
	ds_read_b128 v[228:231], v135
	ds_read_b128 v[232:235], v135 offset:1024
	ds_read_b128 v[236:239], v135 offset:2048
	ds_read_b128 v[240:243], v135 offset:3072
	s_waitcnt vmcnt(0)
	s_barrier
	s_setprio 1
	s_waitcnt lgkmcnt(0)
	s_bitcmp1_b32 s100, 0
	s_cbranch_scc1 .Lg2p_skip14
	v_mfma_f32_16x16x32_f16 v[94:97], v[228:231], v[10:13], v[94:97]
	v_mfma_f32_16x16x32_f16 v[10:13], v[236:239], v[10:13], v[168:171]
	v_mfma_f32_16x16x32_f16 v[126:129], v[240:243], v[14:17], v[10:13]
	v_mfma_f32_16x16x32_f16 v[10:13], v[228:231], v[18:21], v[172:175]
	v_mfma_f32_16x16x32_f16 v[114:117], v[232:235], v[22:25], v[10:13]
	v_mfma_f32_16x16x32_f16 v[10:13], v[236:239], v[18:21], v[176:179]
	v_mfma_f32_16x16x32_f16 v[118:121], v[240:243], v[22:25], v[10:13]
	v_mfma_f32_16x16x32_f16 v[10:13], v[228:231], v[26:29], v[184:187]
	v_mfma_f32_16x16x32_f16 v[106:109], v[232:235], v[30:33], v[10:13]
	v_mfma_f32_16x16x32_f16 v[10:13], v[236:239], v[26:29], v[188:191]
	v_mfma_f32_16x16x32_f16 v[110:113], v[240:243], v[30:33], v[10:13]
	v_mfma_f32_16x16x32_f16 v[10:13], v[228:231], v[216:219], v[192:195]
	v_mfma_f32_16x16x32_f16 v[122:125], v[232:235], v[14:17], v[94:97]
	v_mfma_f32_16x16x32_f16 v[94:97], v[232:235], v[224:227], v[10:13]
	v_mfma_f32_16x16x32_f16 v[10:13], v[236:239], v[216:219], v[196:199]
	v_mfma_f32_16x16x32_f16 v[102:105], v[240:243], v[224:227], v[10:13]
.Lg2p_skip14:
	s_setprio 0
	s_barrier
	ds_read_b128 v[168:171], v134 offset:49152
	ds_read_b128 v[134:137], v134 offset:50176
	ds_read_b128 v[172:175], v133 offset:49152
	ds_read_b128 v[176:179], v133 offset:50176
	ds_read_b128 v[184:187], v131 offset:49152
	ds_read_b128 v[188:191], v131 offset:50176
	ds_read_b128 v[192:195], v130 offset:49152
	ds_read_b128 v[196:199], v130 offset:50176
	s_barrier
	s_setprio 1
	s_waitcnt lgkmcnt(0)
	s_bitcmp1_b32 s100, 1
	s_cbranch_scc1 .Lg2p_skip15
	v_mfma_f32_16x16x32_f16 v[10:13], v[2:5], v[168:171], v[62:65]
	v_mfma_f32_16x16x32_f16 v[26:29], v[6:9], v[134:137], v[10:13]
	v_mfma_f32_16x16x32_f16 v[10:13], v[208:211], v[168:171], v[58:61]
	v_mfma_f32_16x16x32_f16 v[30:33], v[212:215], v[134:137], v[10:13]
	v_mfma_f32_16x16x32_f16 v[10:13], v[2:5], v[172:175], v[54:57]
	v_mfma_f32_16x16x32_f16 v[18:21], v[6:9], v[176:179], v[10:13]
	v_mfma_f32_16x16x32_f16 v[10:13], v[208:211], v[172:175], v[50:53]
	v_mfma_f32_16x16x32_f16 v[22:25], v[212:215], v[176:179], v[10:13]
	v_mfma_f32_16x16x32_f16 v[10:13], v[2:5], v[184:187], v[46:49]
	v_mfma_f32_16x16x32_f16 v[2:5], v[2:5], v[192:195], v[38:41]
	v_mfma_f32_16x16x32_f16 v[10:13], v[6:9], v[188:191], v[10:13]
	v_mfma_f32_16x16x32_f16 v[14:17], v[208:211], v[184:187], v[42:45]
	v_mfma_f32_16x16x32_f16 v[2:5], v[6:9], v[196:199], v[2:5]
	v_mfma_f32_16x16x32_f16 v[6:9], v[208:211], v[192:195], v[138:141]
	v_mfma_f32_16x16x32_f16 v[14:17], v[212:215], v[188:191], v[14:17]
	v_mfma_f32_16x16x32_f16 v[6:9], v[212:215], v[196:199], v[6:9]
.Lg2p_skip15:
	s_setprio 0
	s_setprio 1
	s_bitcmp1_b32 s100, 1
	s_cbranch_scc1 .Lg2p_skip16
	v_mfma_f32_16x16x32_f16 v[34:37], v[228:231], v[168:171], v[34:37]
	v_mfma_f32_16x16x32_f16 v[58:61], v[232:235], v[134:137], v[34:37]
	v_mfma_f32_16x16x32_f16 v[34:37], v[236:239], v[168:171], v[142:145]
	v_mfma_f32_16x16x32_f16 v[62:65], v[240:243], v[134:137], v[34:37]
	v_mfma_f32_16x16x32_f16 v[34:37], v[228:231], v[172:175], v[154:157]
	v_mfma_f32_16x16x32_f16 v[50:53], v[232:235], v[176:179], v[34:37]
	v_mfma_f32_16x16x32_f16 v[34:37], v[236:239], v[172:175], v[158:161]
	v_mfma_f32_16x16x32_f16 v[54:57], v[240:243], v[176:179], v[34:37]
	v_mfma_f32_16x16x32_f16 v[34:37], v[228:231], v[184:187], v[164:167]
	v_mfma_f32_16x16x32_f16 v[42:45], v[232:235], v[188:191], v[34:37]
	v_mfma_f32_16x16x32_f16 v[34:37], v[236:239], v[184:187], v[220:223]
	v_mfma_f32_16x16x32_f16 v[46:49], v[240:243], v[188:191], v[34:37]
	v_mfma_f32_16x16x32_f16 v[34:37], v[228:231], v[192:195], v[204:207]
	v_mfma_f32_16x16x32_f16 v[38:41], v[236:239], v[192:195], v[200:203]
	v_mfma_f32_16x16x32_f16 v[34:37], v[232:235], v[196:199], v[34:37]
	v_mfma_f32_16x16x32_f16 v[38:41], v[240:243], v[196:199], v[38:41]
